# half of the expert-weight conversion moved out of phase 2 into the attention loop (register-only transposition, staggered across waves)
# speedup vs baseline: 1.0062x; 1.0062x over previous
; #define LAS __attribute__((address_space(3)))
; __device__ __forceinline__ void convert_experts(Frame& F, int lo, int hi) {
;     const int gw = F.vcu * 8 + F.wave, NGW = F.G * 8;
;     LAS unsigned char* scr = F.lds + F.wave * 16384;
;     unsigned char* W1t = WSP(F, WS_W1T, unsigned char); unsigned char* W2t = WSP(F, WS_W2T, unsigned char);
;     const float* weg = F.a->in[I_WEG]; const float* weu = F.a->in[I_WEU]; const float* wed = F.a->in[I_WED];
;     const float* wsg = F.a->in[I_WSG]; const float* wsu = F.a->in[I_WSU]; const float* wsd = F.a->in[I_WSD];
;     ...
;     constexpr int NPAIRS = CONV_ITEMS / 2;
;     (void)lo; (void)hi;
;     ...
;     if (gw < NPAIRS) {
;         const int ns = 2 * ((NPAIRS - gw + NGW - 1) / NGW);
;         int sq = 0, r = CONV_RIDX(0);
;         TItem tc, tn; CONV_DESC(r, tc); tn = tc;
;         int p = 0; bool first = true;
;         titem_issue(tc, F.lane, scr);
;         for (;;) {
;             const bool more = sq + 1 < ns; const int rn = more ? CONV_RIDX(sq + 1) : r;
;             if (more) { CONV_DESC(rn, tn); titem_issue(tn, F.lane, scr + (p ^ 1) * 8192); }
;             if (!more) asm volatile("s_waitcnt vmcnt(0)" ::: "memory");
;             else if (first) asm volatile("s_waitcnt vmcnt(8)" ::: "memory");
;             else asm volatile("s_waitcnt vmcnt(12)" ::: "memory");
;             titem_finish(tc, F.lane, scr + p * 8192);
;             asm volatile("s_waitcnt lgkmcnt(0)" ::: "memory");
;             if (!more) break;
;             tc = tn; r = rn; ++sq; p ^= 1; first = false;
;         }
;     }
; __global__ void __launch_bounds__(NTHR, 2) hybrid_fwd(Args args) {
;     ...
;         const bool conv_first = (blockIdx.x >> 3) & 1;
;         if (conv_first && rep == 0) { Frame F = make_frame(lds); convert_experts(F, 0, CONV_ITEMS); }
.LBB0_143:
	s_cmp_lt_i32 s62, 3
	s_cselect_b64 s[6:7], -1, 0
	s_and_b64 s[6:7], s[6:7], s[4:5]
	s_andn2_b64 vcc, exec, s[6:7]
	s_cbranch_vccnz .LBB0_248
	s_bitcmp0_b32 s2, 3
	s_waitcnt lgkmcnt(0)
	s_cselect_b64 s[20:21], -1, 0
	s_ashr_i32 s40, s2, 31
	s_lshr_b32 s3, s40, 29
	s_add_i32 s4, s2, s3
	s_ashr_i32 s3, s4, 3
	s_and_b32 s4, s4, -8
	s_sub_i32 s33, s2, s4
	s_add_u32 s22, s0, 0xd0
	s_addc_u32 s23, s1, 0
	s_and_b64 vcc, exec, s[20:21]
	s_cbranch_vccnz .LBB0_187
	s_load_dword s8, s[0:1], 0xd0
	s_load_dwordx8 s[72:79], s[0:1], 0x80
	s_load_dwordx4 s[80:83], s[0:1], 0xa0
	s_load_dwordx2 s[84:85], s[0:1], 0xc0
	v_and_b32_e32 v1, 63, v0
	v_lshrrev_b32_e32 v2, 3, v1
	v_and_b32_e32 v3, 7, v1
	v_lshlrev_b32_e32 v4, 4, v3
	v_lshlrev_b32_e32 v5, 4, v2
	v_readfirstlane_b32 s9, v0
	s_waitcnt lgkmcnt(0)
	s_lshr_b32 s9, s9, 6
	s_and_b32 s10, s8, 7
	s_mov_b32 s11, s2
	s_cmp_lg_u32 s10, 0
	s_cbranch_scc1 .Lcv1_vcu
	s_and_b32 s10, s2, 7
	s_lshr_b32 s11, s8, 3
	s_mul_i32 s11, s11, s10
	s_lshr_b32 s10, s2, 3
	s_add_u32 s11, s11, s10
.Lcv1_vcu:
	s_lshl_b32 s11, s11, 3
	s_add_u32 s89, s11, s9
	s_lshl_b32 s71, s8, 3
	s_mul_i32 s10, s71, 12
	s_add_u32 s89, s89, s10
	s_mov_b32 s69, s89
	s_add_u32 s86, s84, 0x9180000
	s_addc_u32 s87, s85, 0
	s_add_u32 s84, s84, 0x1100000
	s_addc_u32 s85, s85, 0
	s_mov_b32 s90, 0xc2b8aa3b
	s_cmp_ge_u32 s89, 49344
	s_cbranch_scc1 .Lcv1_done
	s_cmp_lt_u32 s69, 49344
	s_cbranch_scc0 .Lcv1_dummyA1
	s_lshr_b32 s10, s69, 6
	s_and_b32 s12, s69, 63
	s_mul_hi_u32 s14, s10, 0xaaaaaaab
	s_lshr_b32 s14, s14, 1
	s_mul_i32 s11, s14, 3
	s_sub_u32 s11, s10, s11
	s_cmp_lt_u32 s14, 256
	s_cselect_b32 s10, s14, 0
	s_cselect_b64 s[44:45], -1, 0
	s_lshl_b32 s10, s10, 20
	s_cmp_eq_u32 s11, 2
	s_cbranch_scc1 .Lcv1_downA1
	s_cmp_eq_u32 s11, 0
	s_cselect_b64 s[4:5], s[72:73], s[74:75]
	s_cselect_b64 s[38:39], s[78:79], s[80:81]
	s_mov_b32 s94, 0xc3317218
	s_cselect_b32 s94, s90, s94
	s_cmp_lg_u64 s[44:45], 0
	s_cselect_b64 s[4:5], s[4:5], s[38:39]
	s_lshr_b32 s38, s12, 3
	s_and_b32 s39, s12, 7
	s_lshl_b32 s8, s38, 17
	s_add_u32 s10, s10, s8
	s_lshl_b32 s8, s39, 7
	s_add_u32 s10, s10, s8
	s_add_u32 s4, s4, s10
	s_addc_u32 s5, s5, 0
	s_lshl_b32 s14, s14, 19
	s_lshr_b32 s8, s39, 2
	s_lshl_b32 s8, s8, 18
	s_add_u32 s14, s14, s8
	s_and_b32 s8, s39, 3
	s_lshl_b32 s8, s8, 15
	s_add_u32 s14, s14, s8
	s_lshl_b32 s8, s11, 17
	s_add_u32 s14, s14, s8
	s_lshl_b32 s8, s38, 7
	s_add_u32 s14, s14, s8
	s_add_u32 s92, s84, s14
	s_addc_u32 s93, s85, 0
	s_movk_i32 s25, 0x400
	s_movk_i32 s27, 0x1000
	s_movk_i32 s8, 0x400
	s_movk_i32 s9, 0x4000
	s_branch .Lcv1_goA1
.Lcv1_downA1:
	s_cmp_lg_u64 s[44:45], 0
	s_cselect_b64 s[4:5], s[76:77], s[82:83]
	s_mov_b32 s94, 0x42800000
	s_lshr_b32 s38, s12, 5
	s_and_b32 s39, s12, 31
	s_lshl_b32 s8, s38, 19
	s_add_u32 s10, s10, s8
	s_lshl_b32 s8, s39, 7
	s_add_u32 s10, s10, s8
	s_add_u32 s4, s4, s10
	s_addc_u32 s5, s5, 0
	s_lshl_b32 s14, s14, 18
	s_lshl_b32 s8, s39, 13
	s_add_u32 s14, s14, s8
	s_lshl_b32 s8, s38, 7
	s_add_u32 s14, s14, s8
	s_add_u32 s92, s86, s14
	s_addc_u32 s93, s87, 0
	s_movk_i32 s25, 0x100
	s_movk_i32 s27, 0x400
	s_movk_i32 s8, 0x1000
	s_mov_b32 s9, 0x10000
	s_branch .Lcv1_goA1
.Lcv1_dummyA1:
	s_mov_b64 s[4:5], s[72:73]
	s_mov_b32 s8, 0
	s_mov_b32 s9, 0
.Lcv1_goA1:
	s_mov_b32 s95, s94
	v_mad_u32_u24 v6, v2, s9, v4
	global_load_dwordx4 v[32:35], v6, s[4:5] nt
	s_add_u32 s4, s4, s8
	s_addc_u32 s5, s5, 0
	global_load_dwordx4 v[36:39], v6, s[4:5] nt
	s_add_u32 s4, s4, s8
	s_addc_u32 s5, s5, 0
	global_load_dwordx4 v[40:43], v6, s[4:5] nt
	s_add_u32 s4, s4, s8
	s_addc_u32 s5, s5, 0
	global_load_dwordx4 v[44:47], v6, s[4:5] nt
	s_add_u32 s4, s4, s8
	s_addc_u32 s5, s5, 0
	global_load_dwordx4 v[48:51], v6, s[4:5] nt
	s_add_u32 s4, s4, s8
	s_addc_u32 s5, s5, 0
	global_load_dwordx4 v[52:55], v6, s[4:5] nt
	s_add_u32 s4, s4, s8
	s_addc_u32 s5, s5, 0
	global_load_dwordx4 v[56:59], v6, s[4:5] nt
	s_add_u32 s4, s4, s8
	s_addc_u32 s5, s5, 0
	global_load_dwordx4 v[60:63], v6, s[4:5] nt
	s_add_u32 s4, s4, s8
	s_addc_u32 s5, s5, 0
	global_load_dwordx4 v[64:67], v6, s[4:5] nt
	s_add_u32 s4, s4, s8
	s_addc_u32 s5, s5, 0
	global_load_dwordx4 v[68:71], v6, s[4:5] nt
	s_add_u32 s4, s4, s8
	s_addc_u32 s5, s5, 0
	global_load_dwordx4 v[72:75], v6, s[4:5] nt
	s_add_u32 s4, s4, s8
	s_addc_u32 s5, s5, 0
	global_load_dwordx4 v[76:79], v6, s[4:5] nt
	s_add_u32 s4, s4, s8
	s_addc_u32 s5, s5, 0
	global_load_dwordx4 v[80:83], v6, s[4:5] nt
	s_add_u32 s4, s4, s8
	s_addc_u32 s5, s5, 0
	global_load_dwordx4 v[84:87], v6, s[4:5] nt
	s_add_u32 s4, s4, s8
	s_addc_u32 s5, s5, 0
	global_load_dwordx4 v[88:91], v6, s[4:5] nt
	s_add_u32 s4, s4, s8
	s_addc_u32 s5, s5, 0
	global_load_dwordx4 v[92:95], v6, s[4:5] nt
	s_add_u32 s69, s69, s71
	s_cmp_lt_u32 s69, 49344
	s_cbranch_scc0 .Lcv1_dummyB2
	s_lshr_b32 s10, s69, 6
	s_and_b32 s12, s69, 63
	s_mul_hi_u32 s14, s10, 0xaaaaaaab
	s_lshr_b32 s14, s14, 1
	s_mul_i32 s11, s14, 3
	s_sub_u32 s11, s10, s11
	s_cmp_lt_u32 s14, 256
	s_cselect_b32 s10, s14, 0
	s_cselect_b64 s[44:45], -1, 0
	s_lshl_b32 s10, s10, 20
	s_cmp_eq_u32 s11, 2
	s_cbranch_scc1 .Lcv1_downB2
	s_cmp_eq_u32 s11, 0
	s_cselect_b64 s[4:5], s[72:73], s[74:75]
	s_cselect_b64 s[38:39], s[78:79], s[80:81]
	s_mov_b32 s98, 0xc3317218
	s_cselect_b32 s98, s90, s98
	s_cmp_lg_u64 s[44:45], 0
	s_cselect_b64 s[4:5], s[4:5], s[38:39]
	s_lshr_b32 s38, s12, 3
	s_and_b32 s39, s12, 7
	s_lshl_b32 s8, s38, 17
	s_add_u32 s10, s10, s8
	s_lshl_b32 s8, s39, 7
	s_add_u32 s10, s10, s8
	s_add_u32 s4, s4, s10
	s_addc_u32 s5, s5, 0
	s_lshl_b32 s14, s14, 19
	s_lshr_b32 s8, s39, 2
	s_lshl_b32 s8, s8, 18
	s_add_u32 s14, s14, s8
	s_and_b32 s8, s39, 3
	s_lshl_b32 s8, s8, 15
	s_add_u32 s14, s14, s8
	s_lshl_b32 s8, s11, 17
	s_add_u32 s14, s14, s8
	s_lshl_b32 s8, s38, 7
	s_add_u32 s14, s14, s8
	s_add_u32 s96, s84, s14
	s_addc_u32 s97, s85, 0
	s_movk_i32 s32, 0x400
	s_movk_i32 s41, 0x1000
	s_movk_i32 s8, 0x400
	s_movk_i32 s9, 0x4000
	s_branch .Lcv1_goB2
.Lcv1_downB2:
	s_cmp_lg_u64 s[44:45], 0
	s_cselect_b64 s[4:5], s[76:77], s[82:83]
	s_mov_b32 s98, 0x42800000
	s_lshr_b32 s38, s12, 5
	s_and_b32 s39, s12, 31
	s_lshl_b32 s8, s38, 19
	s_add_u32 s10, s10, s8
	s_lshl_b32 s8, s39, 7
	s_add_u32 s10, s10, s8
	s_add_u32 s4, s4, s10
	s_addc_u32 s5, s5, 0
	s_lshl_b32 s14, s14, 18
	s_lshl_b32 s8, s39, 13
	s_add_u32 s14, s14, s8
	s_lshl_b32 s8, s38, 7
	s_add_u32 s14, s14, s8
	s_add_u32 s96, s86, s14
	s_addc_u32 s97, s87, 0
	s_movk_i32 s32, 0x100
	s_movk_i32 s41, 0x400
	s_movk_i32 s8, 0x1000
	s_mov_b32 s9, 0x10000
	s_branch .Lcv1_goB2

; __device__ __forceinline__ void convert_experts(Frame& F, int lo, int hi) {
;     ...
;     constexpr int NPAIRS = CONV_ITEMS / 2;
;     (void)lo; (void)hi;
;     ...
;     if (gw < NPAIRS) {
;         const int ns = 2 * ((NPAIRS - gw + NGW - 1) / NGW);
;         int sq = 0, r = CONV_RIDX(0);
;         TItem tc, tn; CONV_DESC(r, tc); tn = tc;
;         int p = 0; bool first = true;
;         titem_issue(tc, F.lane, scr);
;         for (;;) {
;             const bool more = sq + 1 < ns; const int rn = more ? CONV_RIDX(sq + 1) : r;
;             if (more) { CONV_DESC(rn, tn); titem_issue(tn, F.lane, scr + (p ^ 1) * 8192); }
;             if (!more) asm volatile("s_waitcnt vmcnt(0)" ::: "memory");
;             else if (first) asm volatile("s_waitcnt vmcnt(8)" ::: "memory");
;             else asm volatile("s_waitcnt vmcnt(12)" ::: "memory");
;             titem_finish(tc, F.lane, scr + p * 8192);
;             asm volatile("s_waitcnt lgkmcnt(0)" ::: "memory");
;             if (!more) break;
;             tc = tn; r = rn; ++sq; p ^= 1; first = false;
;         }
.Lcv1_goB2:
	s_mov_b32 s99, s98
	v_mad_u32_u24 v6, v2, s9, v4
	global_load_dwordx4 v[96:99], v6, s[4:5] nt
	s_add_u32 s4, s4, s8
	s_addc_u32 s5, s5, 0
	global_load_dwordx4 v[100:103], v6, s[4:5] nt
	s_add_u32 s4, s4, s8
	s_addc_u32 s5, s5, 0
	global_load_dwordx4 v[104:107], v6, s[4:5] nt
	s_add_u32 s4, s4, s8
	s_addc_u32 s5, s5, 0
	global_load_dwordx4 v[108:111], v6, s[4:5] nt
	s_add_u32 s4, s4, s8
	s_addc_u32 s5, s5, 0
	global_load_dwordx4 v[112:115], v6, s[4:5] nt
	s_add_u32 s4, s4, s8
	s_addc_u32 s5, s5, 0
	global_load_dwordx4 v[116:119], v6, s[4:5] nt
	s_add_u32 s4, s4, s8
	s_addc_u32 s5, s5, 0
	global_load_dwordx4 v[120:123], v6, s[4:5] nt
	s_add_u32 s4, s4, s8
	s_addc_u32 s5, s5, 0
	global_load_dwordx4 v[124:127], v6, s[4:5] nt
	s_add_u32 s4, s4, s8
	s_addc_u32 s5, s5, 0
	global_load_dwordx4 v[128:131], v6, s[4:5] nt
	s_add_u32 s4, s4, s8
	s_addc_u32 s5, s5, 0
	global_load_dwordx4 v[132:135], v6, s[4:5] nt
	s_add_u32 s4, s4, s8
	s_addc_u32 s5, s5, 0
	global_load_dwordx4 v[136:139], v6, s[4:5] nt
	s_add_u32 s4, s4, s8
	s_addc_u32 s5, s5, 0
	global_load_dwordx4 v[140:143], v6, s[4:5] nt
	s_add_u32 s4, s4, s8
	s_addc_u32 s5, s5, 0
	global_load_dwordx4 v[144:147], v6, s[4:5] nt
	s_add_u32 s4, s4, s8
	s_addc_u32 s5, s5, 0
	global_load_dwordx4 v[148:151], v6, s[4:5] nt
	s_add_u32 s4, s4, s8
	s_addc_u32 s5, s5, 0
	global_load_dwordx4 v[152:155], v6, s[4:5] nt
	s_add_u32 s4, s4, s8
	s_addc_u32 s5, s5, 0
	global_load_dwordx4 v[156:159], v6, s[4:5] nt
	s_add_u32 s69, s69, s71
	s_cmp_lt_u32 s69, 49344
	s_cbranch_scc0 .Lcv1_dummyC3
	s_lshr_b32 s10, s69, 6
	s_and_b32 s12, s69, 63
	s_mul_hi_u32 s14, s10, 0xaaaaaaab
	s_lshr_b32 s14, s14, 1
	s_mul_i32 s11, s14, 3
	s_sub_u32 s11, s10, s11
	s_cmp_lt_u32 s14, 256
	s_cselect_b32 s10, s14, 0
	s_cselect_b64 s[44:45], -1, 0
	s_lshl_b32 s10, s10, 20
	s_cmp_eq_u32 s11, 2
	s_cbranch_scc1 .Lcv1_downC3
	s_cmp_eq_u32 s11, 0
	s_cselect_b64 s[4:5], s[72:73], s[74:75]
	s_cselect_b64 s[38:39], s[78:79], s[80:81]
	s_mov_b32 s64, 0xc3317218
	s_cselect_b32 s64, s90, s64
	s_cmp_lg_u64 s[44:45], 0
	s_cselect_b64 s[4:5], s[4:5], s[38:39]
	s_lshr_b32 s38, s12, 3
	s_and_b32 s39, s12, 7
	s_lshl_b32 s8, s38, 17
	s_add_u32 s10, s10, s8
	s_lshl_b32 s8, s39, 7
	s_add_u32 s10, s10, s8
	s_add_u32 s4, s4, s10
	s_addc_u32 s5, s5, 0
	s_lshl_b32 s14, s14, 19
	s_lshr_b32 s8, s39, 2
	s_lshl_b32 s8, s8, 18
	s_add_u32 s14, s14, s8
	s_and_b32 s8, s39, 3
	s_lshl_b32 s8, s8, 15
	s_add_u32 s14, s14, s8
	s_lshl_b32 s8, s11, 17
	s_add_u32 s14, s14, s8
	s_lshl_b32 s8, s38, 7
	s_add_u32 s14, s14, s8
	s_add_u32 s100, s84, s14
	s_addc_u32 s101, s85, 0
	s_movk_i32 s55, 0x400
	s_movk_i32 s58, 0x1000
	s_movk_i32 s8, 0x400
	s_movk_i32 s9, 0x4000
	s_branch .Lcv1_goC3
.Lcv1_downC3:
	s_cmp_lg_u64 s[44:45], 0
	s_cselect_b64 s[4:5], s[76:77], s[82:83]
	s_mov_b32 s64, 0x42800000
	s_lshr_b32 s38, s12, 5
	s_and_b32 s39, s12, 31
	s_lshl_b32 s8, s38, 19
	s_add_u32 s10, s10, s8
	s_lshl_b32 s8, s39, 7
	s_add_u32 s10, s10, s8
	s_add_u32 s4, s4, s10
	s_addc_u32 s5, s5, 0
	s_lshl_b32 s14, s14, 18
	s_lshl_b32 s8, s39, 13
	s_add_u32 s14, s14, s8
	s_lshl_b32 s8, s38, 7
	s_add_u32 s14, s14, s8
	s_add_u32 s100, s86, s14
	s_addc_u32 s101, s87, 0
	s_movk_i32 s55, 0x100
	s_movk_i32 s58, 0x400
	s_movk_i32 s8, 0x1000
	s_mov_b32 s9, 0x10000
	s_branch .Lcv1_goC3

; __device__ __forceinline__ void convert_experts(Frame& F, int lo, int hi) {
;     ...
;     constexpr int NPAIRS = CONV_ITEMS / 2;
;     (void)lo; (void)hi;
;     ...
;     if (gw < NPAIRS) {
;         const int ns = 2 * ((NPAIRS - gw + NGW - 1) / NGW);
;         int sq = 0, r = CONV_RIDX(0);
;         TItem tc, tn; CONV_DESC(r, tc); tn = tc;
;         int p = 0; bool first = true;
;         titem_issue(tc, F.lane, scr);
;         for (;;) {
;             const bool more = sq + 1 < ns; const int rn = more ? CONV_RIDX(sq + 1) : r;
;             if (more) { CONV_DESC(rn, tn); titem_issue(tn, F.lane, scr + (p ^ 1) * 8192); }
;             if (!more) asm volatile("s_waitcnt vmcnt(0)" ::: "memory");
;             else if (first) asm volatile("s_waitcnt vmcnt(8)" ::: "memory");
;             else asm volatile("s_waitcnt vmcnt(12)" ::: "memory");
;             titem_finish(tc, F.lane, scr + p * 8192);
;             asm volatile("s_waitcnt lgkmcnt(0)" ::: "memory");
;             if (!more) break;
;             tc = tn; r = rn; ++sq; p ^= 1; first = false;
;         }
.Lcv1_goC3:
	s_mov_b32 s65, s64
	v_mad_u32_u24 v6, v2, s9, v4
	global_load_dwordx4 v[164:167], v6, s[4:5] nt
	s_add_u32 s4, s4, s8
	s_addc_u32 s5, s5, 0
	global_load_dwordx4 v[168:171], v6, s[4:5] nt
	s_add_u32 s4, s4, s8
	s_addc_u32 s5, s5, 0
	global_load_dwordx4 v[172:175], v6, s[4:5] nt
	s_add_u32 s4, s4, s8
	s_addc_u32 s5, s5, 0
	global_load_dwordx4 v[176:179], v6, s[4:5] nt
	s_add_u32 s4, s4, s8
	s_addc_u32 s5, s5, 0
	global_load_dwordx4 v[180:183], v6, s[4:5] nt
	s_add_u32 s4, s4, s8
	s_addc_u32 s5, s5, 0
	global_load_dwordx4 v[184:187], v6, s[4:5] nt
	s_add_u32 s4, s4, s8
	s_addc_u32 s5, s5, 0
	global_load_dwordx4 v[188:191], v6, s[4:5] nt
	s_add_u32 s4, s4, s8
	s_addc_u32 s5, s5, 0
	global_load_dwordx4 v[192:195], v6, s[4:5] nt
	s_add_u32 s4, s4, s8
	s_addc_u32 s5, s5, 0
	global_load_dwordx4 v[196:199], v6, s[4:5] nt
	s_add_u32 s4, s4, s8
	s_addc_u32 s5, s5, 0
	global_load_dwordx4 v[200:203], v6, s[4:5] nt
	s_add_u32 s4, s4, s8
	s_addc_u32 s5, s5, 0
	global_load_dwordx4 v[204:207], v6, s[4:5] nt
	s_add_u32 s4, s4, s8
	s_addc_u32 s5, s5, 0
	global_load_dwordx4 v[208:211], v6, s[4:5] nt
	s_add_u32 s4, s4, s8
	s_addc_u32 s5, s5, 0
	global_load_dwordx4 v[212:215], v6, s[4:5] nt
	s_add_u32 s4, s4, s8
	s_addc_u32 s5, s5, 0
	global_load_dwordx4 v[216:219], v6, s[4:5] nt
	s_add_u32 s4, s4, s8
	s_addc_u32 s5, s5, 0
	global_load_dwordx4 v[220:223], v6, s[4:5] nt
	s_add_u32 s4, s4, s8
	s_addc_u32 s5, s5, 0
	global_load_dwordx4 v[224:227], v6, s[4:5] nt
	s_add_u32 s69, s69, s71
.Lcv1_loop:
	s_cmp_ge_u32 s89, 49344
	s_cbranch_scc1 .Lcv1_done
	s_waitcnt vmcnt(32)
	v_pk_mul_f32 v[32:33], v[32:33], s[94:95]
	v_pk_mul_f32 v[34:35], v[34:35], s[94:95]
	v_pk_mul_f32 v[36:37], v[36:37], s[94:95]
	v_pk_mul_f32 v[38:39], v[38:39], s[94:95]
	v_pk_mul_f32 v[40:41], v[40:41], s[94:95]
	v_pk_mul_f32 v[42:43], v[42:43], s[94:95]
	v_pk_mul_f32 v[44:45], v[44:45], s[94:95]
	v_pk_mul_f32 v[46:47], v[46:47], s[94:95]
	v_pk_mul_f32 v[48:49], v[48:49], s[94:95]
	v_pk_mul_f32 v[50:51], v[50:51], s[94:95]
	v_pk_mul_f32 v[52:53], v[52:53], s[94:95]
	v_pk_mul_f32 v[54:55], v[54:55], s[94:95]
	v_pk_mul_f32 v[56:57], v[56:57], s[94:95]
	v_pk_mul_f32 v[58:59], v[58:59], s[94:95]
	v_pk_mul_f32 v[60:61], v[60:61], s[94:95]
	v_pk_mul_f32 v[62:63], v[62:63], s[94:95]
	v_pk_mul_f32 v[64:65], v[64:65], s[94:95]
	v_pk_mul_f32 v[66:67], v[66:67], s[94:95]
	v_pk_mul_f32 v[68:69], v[68:69], s[94:95]
	v_pk_mul_f32 v[70:71], v[70:71], s[94:95]
	v_pk_mul_f32 v[72:73], v[72:73], s[94:95]
	v_pk_mul_f32 v[74:75], v[74:75], s[94:95]
	v_pk_mul_f32 v[76:77], v[76:77], s[94:95]
	v_pk_mul_f32 v[78:79], v[78:79], s[94:95]
	v_pk_mul_f32 v[80:81], v[80:81], s[94:95]
	v_pk_mul_f32 v[82:83], v[82:83], s[94:95]
	v_pk_mul_f32 v[84:85], v[84:85], s[94:95]
	v_pk_mul_f32 v[86:87], v[86:87], s[94:95]
	v_pk_mul_f32 v[88:89], v[88:89], s[94:95]
	v_pk_mul_f32 v[90:91], v[90:91], s[94:95]
	v_pk_mul_f32 v[92:93], v[92:93], s[94:95]
	v_pk_mul_f32 v[94:95], v[94:95], s[94:95]
	v_mad_u32_u24 v24, v3, s27, v5
	v_cvt_pk_fp8_f32 v8, v32, v36
	v_cvt_pk_fp8_f32 v9, v48, v52
	v_cvt_pk_fp8_f32 v10, v64, v68
	v_cvt_pk_fp8_f32 v11, v80, v84
	v_cvt_pk_fp8_f32 v12, v33, v37
	v_cvt_pk_fp8_f32 v13, v49, v53
	v_cvt_pk_fp8_f32 v14, v65, v69
	v_cvt_pk_fp8_f32 v15, v81, v85
	v_cvt_pk_fp8_f32 v16, v34, v38
	v_cvt_pk_fp8_f32 v17, v50, v54
	v_cvt_pk_fp8_f32 v18, v66, v70
	v_cvt_pk_fp8_f32 v19, v82, v86
	v_cvt_pk_fp8_f32 v20, v35, v39
	v_cvt_pk_fp8_f32 v21, v51, v55
	v_cvt_pk_fp8_f32 v22, v67, v71
	v_cvt_pk_fp8_f32 v23, v83, v87
	v_add_u32_e32 v25, s25, v24
	v_add_u32_e32 v26, s25, v25
	v_add_u32_e32 v27, s25, v26
	v_cvt_pk_fp8_f32 v8, v40, v44 op_sel:[0,0,1]
	v_cvt_pk_fp8_f32 v9, v56, v60 op_sel:[0,0,1]
	v_cvt_pk_fp8_f32 v10, v72, v76 op_sel:[0,0,1]
	v_cvt_pk_fp8_f32 v11, v88, v92 op_sel:[0,0,1]
	v_cvt_pk_fp8_f32 v12, v41, v45 op_sel:[0,0,1]
	v_cvt_pk_fp8_f32 v13, v57, v61 op_sel:[0,0,1]
	v_cvt_pk_fp8_f32 v14, v73, v77 op_sel:[0,0,1]
	v_cvt_pk_fp8_f32 v15, v89, v93 op_sel:[0,0,1]
	v_cvt_pk_fp8_f32 v16, v42, v46 op_sel:[0,0,1]
	v_cvt_pk_fp8_f32 v17, v58, v62 op_sel:[0,0,1]
	v_cvt_pk_fp8_f32 v18, v74, v78 op_sel:[0,0,1]
	v_cvt_pk_fp8_f32 v19, v90, v94 op_sel:[0,0,1]
	v_cvt_pk_fp8_f32 v20, v43, v47 op_sel:[0,0,1]
	v_cvt_pk_fp8_f32 v21, v59, v63 op_sel:[0,0,1]
	v_cvt_pk_fp8_f32 v22, v75, v79 op_sel:[0,0,1]
	v_cvt_pk_fp8_f32 v23, v91, v95 op_sel:[0,0,1]
	global_store_dwordx4 v24, v[8:11], s[92:93] nt
	global_store_dwordx4 v25, v[12:15], s[92:93] nt
	global_store_dwordx4 v26, v[16:19], s[92:93] nt
	global_store_dwordx4 v27, v[20:23], s[92:93] nt
	s_add_u32 s89, s89, s71
	s_cmp_lt_u32 s69, 49344
	s_cbranch_scc0 .Lcv1_dummyA4
	s_lshr_b32 s10, s69, 6
	s_and_b32 s12, s69, 63
	s_mul_hi_u32 s14, s10, 0xaaaaaaab
	s_lshr_b32 s14, s14, 1
	s_mul_i32 s11, s14, 3
	s_sub_u32 s11, s10, s11
	s_cmp_lt_u32 s14, 256
	s_cselect_b32 s10, s14, 0
	s_cselect_b64 s[44:45], -1, 0
	s_lshl_b32 s10, s10, 20
	s_cmp_eq_u32 s11, 2
	s_cbranch_scc1 .Lcv1_downA4
	s_cmp_eq_u32 s11, 0
	s_cselect_b64 s[4:5], s[72:73], s[74:75]
	s_cselect_b64 s[38:39], s[78:79], s[80:81]
	s_mov_b32 s94, 0xc3317218
	s_cselect_b32 s94, s90, s94
	s_cmp_lg_u64 s[44:45], 0
	s_cselect_b64 s[4:5], s[4:5], s[38:39]
	s_lshr_b32 s38, s12, 3
	s_and_b32 s39, s12, 7
	s_lshl_b32 s8, s38, 17
	s_add_u32 s10, s10, s8
	s_lshl_b32 s8, s39, 7
	s_add_u32 s10, s10, s8
	s_add_u32 s4, s4, s10
	s_addc_u32 s5, s5, 0
	s_lshl_b32 s14, s14, 19
	s_lshr_b32 s8, s39, 2
	s_lshl_b32 s8, s8, 18
	s_add_u32 s14, s14, s8
	s_and_b32 s8, s39, 3
	s_lshl_b32 s8, s8, 15
	s_add_u32 s14, s14, s8
	s_lshl_b32 s8, s11, 17
	s_add_u32 s14, s14, s8
	s_lshl_b32 s8, s38, 7
	s_add_u32 s14, s14, s8
	s_add_u32 s92, s84, s14
	s_addc_u32 s93, s85, 0
	s_movk_i32 s25, 0x400
	s_movk_i32 s27, 0x1000
	s_movk_i32 s8, 0x400
	s_movk_i32 s9, 0x4000
	s_branch .Lcv1_goA4

; __device__ __forceinline__ void convert_experts(Frame& F, int lo, int hi) {
;     ...
;     constexpr int NPAIRS = CONV_ITEMS / 2;
;     (void)lo; (void)hi;
;     ...
;     if (gw < NPAIRS) {
;         const int ns = 2 * ((NPAIRS - gw + NGW - 1) / NGW);
;         int sq = 0, r = CONV_RIDX(0);
;         TItem tc, tn; CONV_DESC(r, tc); tn = tc;
;         int p = 0; bool first = true;
;         titem_issue(tc, F.lane, scr);
;         for (;;) {
;             const bool more = sq + 1 < ns; const int rn = more ? CONV_RIDX(sq + 1) : r;
;             if (more) { CONV_DESC(rn, tn); titem_issue(tn, F.lane, scr + (p ^ 1) * 8192); }
;             if (!more) asm volatile("s_waitcnt vmcnt(0)" ::: "memory");
;             else if (first) asm volatile("s_waitcnt vmcnt(8)" ::: "memory");
;             else asm volatile("s_waitcnt vmcnt(12)" ::: "memory");
;             titem_finish(tc, F.lane, scr + p * 8192);
;             asm volatile("s_waitcnt lgkmcnt(0)" ::: "memory");
;             if (!more) break;
;             tc = tn; r = rn; ++sq; p ^= 1; first = false;
;         }
.Lcv1_goA4:
	s_mov_b32 s95, s94
	v_mad_u32_u24 v6, v2, s9, v4
	global_load_dwordx4 v[32:35], v6, s[4:5] nt
	s_add_u32 s4, s4, s8
	s_addc_u32 s5, s5, 0
	global_load_dwordx4 v[36:39], v6, s[4:5] nt
	s_add_u32 s4, s4, s8
	s_addc_u32 s5, s5, 0
	global_load_dwordx4 v[40:43], v6, s[4:5] nt
	s_add_u32 s4, s4, s8
	s_addc_u32 s5, s5, 0
	global_load_dwordx4 v[44:47], v6, s[4:5] nt
	s_add_u32 s4, s4, s8
	s_addc_u32 s5, s5, 0
	global_load_dwordx4 v[48:51], v6, s[4:5] nt
	s_add_u32 s4, s4, s8
	s_addc_u32 s5, s5, 0
	global_load_dwordx4 v[52:55], v6, s[4:5] nt
	s_add_u32 s4, s4, s8
	s_addc_u32 s5, s5, 0
	global_load_dwordx4 v[56:59], v6, s[4:5] nt
	s_add_u32 s4, s4, s8
	s_addc_u32 s5, s5, 0
	global_load_dwordx4 v[60:63], v6, s[4:5] nt
	s_add_u32 s4, s4, s8
	s_addc_u32 s5, s5, 0
	global_load_dwordx4 v[64:67], v6, s[4:5] nt
	s_add_u32 s4, s4, s8
	s_addc_u32 s5, s5, 0
	global_load_dwordx4 v[68:71], v6, s[4:5] nt
	s_add_u32 s4, s4, s8
	s_addc_u32 s5, s5, 0
	global_load_dwordx4 v[72:75], v6, s[4:5] nt
	s_add_u32 s4, s4, s8
	s_addc_u32 s5, s5, 0
	global_load_dwordx4 v[76:79], v6, s[4:5] nt
	s_add_u32 s4, s4, s8
	s_addc_u32 s5, s5, 0
	global_load_dwordx4 v[80:83], v6, s[4:5] nt
	s_add_u32 s4, s4, s8
	s_addc_u32 s5, s5, 0
	global_load_dwordx4 v[84:87], v6, s[4:5] nt
	s_add_u32 s4, s4, s8
	s_addc_u32 s5, s5, 0
	global_load_dwordx4 v[88:91], v6, s[4:5] nt
	s_add_u32 s4, s4, s8
	s_addc_u32 s5, s5, 0
	global_load_dwordx4 v[92:95], v6, s[4:5] nt
	s_add_u32 s69, s69, s71
	s_cmp_ge_u32 s89, 49344
	s_cbranch_scc1 .Lcv1_done
	s_waitcnt vmcnt(36)
	v_pk_mul_f32 v[96:97], v[96:97], s[98:99]
	v_pk_mul_f32 v[98:99], v[98:99], s[98:99]
	v_pk_mul_f32 v[100:101], v[100:101], s[98:99]
	v_pk_mul_f32 v[102:103], v[102:103], s[98:99]
	v_pk_mul_f32 v[104:105], v[104:105], s[98:99]
	v_pk_mul_f32 v[106:107], v[106:107], s[98:99]
	v_pk_mul_f32 v[108:109], v[108:109], s[98:99]
	v_pk_mul_f32 v[110:111], v[110:111], s[98:99]
	v_pk_mul_f32 v[112:113], v[112:113], s[98:99]
	v_pk_mul_f32 v[114:115], v[114:115], s[98:99]
	v_pk_mul_f32 v[116:117], v[116:117], s[98:99]
	v_pk_mul_f32 v[118:119], v[118:119], s[98:99]
	v_pk_mul_f32 v[120:121], v[120:121], s[98:99]
	v_pk_mul_f32 v[122:123], v[122:123], s[98:99]
	v_pk_mul_f32 v[124:125], v[124:125], s[98:99]
	v_pk_mul_f32 v[126:127], v[126:127], s[98:99]
	v_pk_mul_f32 v[128:129], v[128:129], s[98:99]
	v_pk_mul_f32 v[130:131], v[130:131], s[98:99]
	v_pk_mul_f32 v[132:133], v[132:133], s[98:99]
	v_pk_mul_f32 v[134:135], v[134:135], s[98:99]
	v_pk_mul_f32 v[136:137], v[136:137], s[98:99]
	v_pk_mul_f32 v[138:139], v[138:139], s[98:99]
	v_pk_mul_f32 v[140:141], v[140:141], s[98:99]
	v_pk_mul_f32 v[142:143], v[142:143], s[98:99]
	v_pk_mul_f32 v[144:145], v[144:145], s[98:99]
	v_pk_mul_f32 v[146:147], v[146:147], s[98:99]
	v_pk_mul_f32 v[148:149], v[148:149], s[98:99]
	v_pk_mul_f32 v[150:151], v[150:151], s[98:99]
	v_pk_mul_f32 v[152:153], v[152:153], s[98:99]
	v_pk_mul_f32 v[154:155], v[154:155], s[98:99]
	v_pk_mul_f32 v[156:157], v[156:157], s[98:99]
	v_pk_mul_f32 v[158:159], v[158:159], s[98:99]
	v_mad_u32_u24 v24, v3, s41, v5
	v_cvt_pk_fp8_f32 v8, v96, v100
	v_cvt_pk_fp8_f32 v9, v112, v116
	v_cvt_pk_fp8_f32 v10, v128, v132
	v_cvt_pk_fp8_f32 v11, v144, v148
	v_cvt_pk_fp8_f32 v12, v97, v101
	v_cvt_pk_fp8_f32 v13, v113, v117
	v_cvt_pk_fp8_f32 v14, v129, v133
	v_cvt_pk_fp8_f32 v15, v145, v149
	v_cvt_pk_fp8_f32 v16, v98, v102
	v_cvt_pk_fp8_f32 v17, v114, v118
	v_cvt_pk_fp8_f32 v18, v130, v134
	v_cvt_pk_fp8_f32 v19, v146, v150
	v_cvt_pk_fp8_f32 v20, v99, v103
	v_cvt_pk_fp8_f32 v21, v115, v119
	v_cvt_pk_fp8_f32 v22, v131, v135
	v_cvt_pk_fp8_f32 v23, v147, v151
	v_add_u32_e32 v25, s32, v24
	v_add_u32_e32 v26, s32, v25
	v_add_u32_e32 v27, s32, v26
	v_cvt_pk_fp8_f32 v8, v104, v108 op_sel:[0,0,1]
	v_cvt_pk_fp8_f32 v9, v120, v124 op_sel:[0,0,1]
	v_cvt_pk_fp8_f32 v10, v136, v140 op_sel:[0,0,1]
	v_cvt_pk_fp8_f32 v11, v152, v156 op_sel:[0,0,1]
	v_cvt_pk_fp8_f32 v12, v105, v109 op_sel:[0,0,1]
	v_cvt_pk_fp8_f32 v13, v121, v125 op_sel:[0,0,1]
	v_cvt_pk_fp8_f32 v14, v137, v141 op_sel:[0,0,1]
	v_cvt_pk_fp8_f32 v15, v153, v157 op_sel:[0,0,1]
	v_cvt_pk_fp8_f32 v16, v106, v110 op_sel:[0,0,1]
	v_cvt_pk_fp8_f32 v17, v122, v126 op_sel:[0,0,1]
	v_cvt_pk_fp8_f32 v18, v138, v142 op_sel:[0,0,1]
	v_cvt_pk_fp8_f32 v19, v154, v158 op_sel:[0,0,1]
	v_cvt_pk_fp8_f32 v20, v107, v111 op_sel:[0,0,1]
	v_cvt_pk_fp8_f32 v21, v123, v127 op_sel:[0,0,1]
	v_cvt_pk_fp8_f32 v22, v139, v143 op_sel:[0,0,1]
	v_cvt_pk_fp8_f32 v23, v155, v159 op_sel:[0,0,1]
	global_store_dwordx4 v24, v[8:11], s[96:97] nt
	global_store_dwordx4 v25, v[12:15], s[96:97] nt
	global_store_dwordx4 v26, v[16:19], s[96:97] nt
	global_store_dwordx4 v27, v[20:23], s[96:97] nt
	s_add_u32 s89, s89, s71
	s_cmp_lt_u32 s69, 49344
	s_cbranch_scc0 .Lcv1_dummyB5
	s_lshr_b32 s10, s69, 6
	s_and_b32 s12, s69, 63
	s_mul_hi_u32 s14, s10, 0xaaaaaaab
	s_lshr_b32 s14, s14, 1
	s_mul_i32 s11, s14, 3
	s_sub_u32 s11, s10, s11
	s_cmp_lt_u32 s14, 256
	s_cselect_b32 s10, s14, 0
	s_cselect_b64 s[44:45], -1, 0
	s_lshl_b32 s10, s10, 20
	s_cmp_eq_u32 s11, 2
	s_cbranch_scc1 .Lcv1_downB5
	s_cmp_eq_u32 s11, 0
	s_cselect_b64 s[4:5], s[72:73], s[74:75]
	s_cselect_b64 s[38:39], s[78:79], s[80:81]
	s_mov_b32 s98, 0xc3317218
	s_cselect_b32 s98, s90, s98
	s_cmp_lg_u64 s[44:45], 0
	s_cselect_b64 s[4:5], s[4:5], s[38:39]
	s_lshr_b32 s38, s12, 3
	s_and_b32 s39, s12, 7
	s_lshl_b32 s8, s38, 17
	s_add_u32 s10, s10, s8
	s_lshl_b32 s8, s39, 7
	s_add_u32 s10, s10, s8
	s_add_u32 s4, s4, s10
	s_addc_u32 s5, s5, 0
	s_lshl_b32 s14, s14, 19
	s_lshr_b32 s8, s39, 2
	s_lshl_b32 s8, s8, 18
	s_add_u32 s14, s14, s8
	s_and_b32 s8, s39, 3
	s_lshl_b32 s8, s8, 15
	s_add_u32 s14, s14, s8
	s_lshl_b32 s8, s11, 17
	s_add_u32 s14, s14, s8
	s_lshl_b32 s8, s38, 7
	s_add_u32 s14, s14, s8
	s_add_u32 s96, s84, s14
	s_addc_u32 s97, s85, 0
	s_movk_i32 s32, 0x400
	s_movk_i32 s41, 0x1000
	s_movk_i32 s8, 0x400
	s_movk_i32 s9, 0x4000
	s_branch .Lcv1_goB5

; __device__ __forceinline__ void convert_experts(Frame& F, int lo, int hi) {
;     ...
;     constexpr int NPAIRS = CONV_ITEMS / 2;
;     (void)lo; (void)hi;
;     ...
;     if (gw < NPAIRS) {
;         const int ns = 2 * ((NPAIRS - gw + NGW - 1) / NGW);
;         int sq = 0, r = CONV_RIDX(0);
;         TItem tc, tn; CONV_DESC(r, tc); tn = tc;
;         int p = 0; bool first = true;
;         titem_issue(tc, F.lane, scr);
;         for (;;) {
;             const bool more = sq + 1 < ns; const int rn = more ? CONV_RIDX(sq + 1) : r;
;             if (more) { CONV_DESC(rn, tn); titem_issue(tn, F.lane, scr + (p ^ 1) * 8192); }
;             if (!more) asm volatile("s_waitcnt vmcnt(0)" ::: "memory");
;             else if (first) asm volatile("s_waitcnt vmcnt(8)" ::: "memory");
;             else asm volatile("s_waitcnt vmcnt(12)" ::: "memory");
;             titem_finish(tc, F.lane, scr + p * 8192);
;             asm volatile("s_waitcnt lgkmcnt(0)" ::: "memory");
;             if (!more) break;
;             tc = tn; r = rn; ++sq; p ^= 1; first = false;
;         }
.Lcv1_goB5:
	s_mov_b32 s99, s98
	v_mad_u32_u24 v6, v2, s9, v4
	global_load_dwordx4 v[96:99], v6, s[4:5] nt
	s_add_u32 s4, s4, s8
	s_addc_u32 s5, s5, 0
	global_load_dwordx4 v[100:103], v6, s[4:5] nt
	s_add_u32 s4, s4, s8
	s_addc_u32 s5, s5, 0
	global_load_dwordx4 v[104:107], v6, s[4:5] nt
	s_add_u32 s4, s4, s8
	s_addc_u32 s5, s5, 0
	global_load_dwordx4 v[108:111], v6, s[4:5] nt
	s_add_u32 s4, s4, s8
	s_addc_u32 s5, s5, 0
	global_load_dwordx4 v[112:115], v6, s[4:5] nt
	s_add_u32 s4, s4, s8
	s_addc_u32 s5, s5, 0
	global_load_dwordx4 v[116:119], v6, s[4:5] nt
	s_add_u32 s4, s4, s8
	s_addc_u32 s5, s5, 0
	global_load_dwordx4 v[120:123], v6, s[4:5] nt
	s_add_u32 s4, s4, s8
	s_addc_u32 s5, s5, 0
	global_load_dwordx4 v[124:127], v6, s[4:5] nt
	s_add_u32 s4, s4, s8
	s_addc_u32 s5, s5, 0
	global_load_dwordx4 v[128:131], v6, s[4:5] nt
	s_add_u32 s4, s4, s8
	s_addc_u32 s5, s5, 0
	global_load_dwordx4 v[132:135], v6, s[4:5] nt
	s_add_u32 s4, s4, s8
	s_addc_u32 s5, s5, 0
	global_load_dwordx4 v[136:139], v6, s[4:5] nt
	s_add_u32 s4, s4, s8
	s_addc_u32 s5, s5, 0
	global_load_dwordx4 v[140:143], v6, s[4:5] nt
	s_add_u32 s4, s4, s8
	s_addc_u32 s5, s5, 0
	global_load_dwordx4 v[144:147], v6, s[4:5] nt
	s_add_u32 s4, s4, s8
	s_addc_u32 s5, s5, 0
	global_load_dwordx4 v[148:151], v6, s[4:5] nt
	s_add_u32 s4, s4, s8
	s_addc_u32 s5, s5, 0
	global_load_dwordx4 v[152:155], v6, s[4:5] nt
	s_add_u32 s4, s4, s8
	s_addc_u32 s5, s5, 0
	global_load_dwordx4 v[156:159], v6, s[4:5] nt
	s_add_u32 s69, s69, s71
	s_cmp_ge_u32 s89, 49344
	s_cbranch_scc1 .Lcv1_done
	s_waitcnt vmcnt(40)
	v_pk_mul_f32 v[164:165], v[164:165], s[64:65]
	v_pk_mul_f32 v[166:167], v[166:167], s[64:65]
	v_pk_mul_f32 v[168:169], v[168:169], s[64:65]
	v_pk_mul_f32 v[170:171], v[170:171], s[64:65]
	v_pk_mul_f32 v[172:173], v[172:173], s[64:65]
	v_pk_mul_f32 v[174:175], v[174:175], s[64:65]
	v_pk_mul_f32 v[176:177], v[176:177], s[64:65]
	v_pk_mul_f32 v[178:179], v[178:179], s[64:65]
	v_pk_mul_f32 v[180:181], v[180:181], s[64:65]
	v_pk_mul_f32 v[182:183], v[182:183], s[64:65]
	v_pk_mul_f32 v[184:185], v[184:185], s[64:65]
	v_pk_mul_f32 v[186:187], v[186:187], s[64:65]
	v_pk_mul_f32 v[188:189], v[188:189], s[64:65]
	v_pk_mul_f32 v[190:191], v[190:191], s[64:65]
	v_pk_mul_f32 v[192:193], v[192:193], s[64:65]
	v_pk_mul_f32 v[194:195], v[194:195], s[64:65]
	v_pk_mul_f32 v[196:197], v[196:197], s[64:65]
	v_pk_mul_f32 v[198:199], v[198:199], s[64:65]
	v_pk_mul_f32 v[200:201], v[200:201], s[64:65]
	v_pk_mul_f32 v[202:203], v[202:203], s[64:65]
	v_pk_mul_f32 v[204:205], v[204:205], s[64:65]
	v_pk_mul_f32 v[206:207], v[206:207], s[64:65]
	v_pk_mul_f32 v[208:209], v[208:209], s[64:65]
	v_pk_mul_f32 v[210:211], v[210:211], s[64:65]
	v_pk_mul_f32 v[212:213], v[212:213], s[64:65]
	v_pk_mul_f32 v[214:215], v[214:215], s[64:65]
	v_pk_mul_f32 v[216:217], v[216:217], s[64:65]
	v_pk_mul_f32 v[218:219], v[218:219], s[64:65]
	v_pk_mul_f32 v[220:221], v[220:221], s[64:65]
	v_pk_mul_f32 v[222:223], v[222:223], s[64:65]
	v_pk_mul_f32 v[224:225], v[224:225], s[64:65]
	v_pk_mul_f32 v[226:227], v[226:227], s[64:65]
	v_mad_u32_u24 v24, v3, s58, v5
	v_cvt_pk_fp8_f32 v8, v164, v168
	v_cvt_pk_fp8_f32 v9, v180, v184
	v_cvt_pk_fp8_f32 v10, v196, v200
	v_cvt_pk_fp8_f32 v11, v212, v216
	v_cvt_pk_fp8_f32 v12, v165, v169
	v_cvt_pk_fp8_f32 v13, v181, v185
	v_cvt_pk_fp8_f32 v14, v197, v201
	v_cvt_pk_fp8_f32 v15, v213, v217
	v_cvt_pk_fp8_f32 v16, v166, v170
	v_cvt_pk_fp8_f32 v17, v182, v186
	v_cvt_pk_fp8_f32 v18, v198, v202
	v_cvt_pk_fp8_f32 v19, v214, v218
	v_cvt_pk_fp8_f32 v20, v167, v171
	v_cvt_pk_fp8_f32 v21, v183, v187
	v_cvt_pk_fp8_f32 v22, v199, v203
	v_cvt_pk_fp8_f32 v23, v215, v219
	v_add_u32_e32 v25, s55, v24
	v_add_u32_e32 v26, s55, v25
	v_add_u32_e32 v27, s55, v26
	v_cvt_pk_fp8_f32 v8, v172, v176 op_sel:[0,0,1]
	v_cvt_pk_fp8_f32 v9, v188, v192 op_sel:[0,0,1]
	v_cvt_pk_fp8_f32 v10, v204, v208 op_sel:[0,0,1]
	v_cvt_pk_fp8_f32 v11, v220, v224 op_sel:[0,0,1]
	v_cvt_pk_fp8_f32 v12, v173, v177 op_sel:[0,0,1]
	v_cvt_pk_fp8_f32 v13, v189, v193 op_sel:[0,0,1]
	v_cvt_pk_fp8_f32 v14, v205, v209 op_sel:[0,0,1]
	v_cvt_pk_fp8_f32 v15, v221, v225 op_sel:[0,0,1]
	v_cvt_pk_fp8_f32 v16, v174, v178 op_sel:[0,0,1]
	v_cvt_pk_fp8_f32 v17, v190, v194 op_sel:[0,0,1]
	v_cvt_pk_fp8_f32 v18, v206, v210 op_sel:[0,0,1]
	v_cvt_pk_fp8_f32 v19, v222, v226 op_sel:[0,0,1]
	v_cvt_pk_fp8_f32 v20, v175, v179 op_sel:[0,0,1]
	v_cvt_pk_fp8_f32 v21, v191, v195 op_sel:[0,0,1]
	v_cvt_pk_fp8_f32 v22, v207, v211 op_sel:[0,0,1]
	v_cvt_pk_fp8_f32 v23, v223, v227 op_sel:[0,0,1]
	global_store_dwordx4 v24, v[8:11], s[100:101] nt
	global_store_dwordx4 v25, v[12:15], s[100:101] nt
	global_store_dwordx4 v26, v[16:19], s[100:101] nt
	global_store_dwordx4 v27, v[20:23], s[100:101] nt
	s_add_u32 s89, s89, s71
	s_cmp_lt_u32 s69, 49344
	s_cbranch_scc0 .Lcv1_dummyC6
	s_lshr_b32 s10, s69, 6
	s_and_b32 s12, s69, 63
	s_mul_hi_u32 s14, s10, 0xaaaaaaab
	s_lshr_b32 s14, s14, 1
	s_mul_i32 s11, s14, 3
	s_sub_u32 s11, s10, s11
	s_cmp_lt_u32 s14, 256
	s_cselect_b32 s10, s14, 0
	s_cselect_b64 s[44:45], -1, 0
	s_lshl_b32 s10, s10, 20
	s_cmp_eq_u32 s11, 2
	s_cbranch_scc1 .Lcv1_downC6
	s_cmp_eq_u32 s11, 0
	s_cselect_b64 s[4:5], s[72:73], s[74:75]
	s_cselect_b64 s[38:39], s[78:79], s[80:81]
	s_mov_b32 s64, 0xc3317218
	s_cselect_b32 s64, s90, s64
	s_cmp_lg_u64 s[44:45], 0
	s_cselect_b64 s[4:5], s[4:5], s[38:39]
	s_lshr_b32 s38, s12, 3
	s_and_b32 s39, s12, 7
	s_lshl_b32 s8, s38, 17
	s_add_u32 s10, s10, s8
	s_lshl_b32 s8, s39, 7
	s_add_u32 s10, s10, s8
	s_add_u32 s4, s4, s10
	s_addc_u32 s5, s5, 0
	s_lshl_b32 s14, s14, 19
	s_lshr_b32 s8, s39, 2
	s_lshl_b32 s8, s8, 18
	s_add_u32 s14, s14, s8
	s_and_b32 s8, s39, 3
	s_lshl_b32 s8, s8, 15
	s_add_u32 s14, s14, s8
	s_lshl_b32 s8, s11, 17
	s_add_u32 s14, s14, s8
	s_lshl_b32 s8, s38, 7
	s_add_u32 s14, s14, s8
	s_add_u32 s100, s84, s14
	s_addc_u32 s101, s85, 0
	s_movk_i32 s55, 0x400
	s_movk_i32 s58, 0x1000
	s_movk_i32 s8, 0x400
	s_movk_i32 s9, 0x4000
	s_branch .Lcv1_goC6

; __device__ __forceinline__ void convert_experts(Frame& F, int lo, int hi) {
;     ...
;         for (;;) {
;             const bool more = sq + 1 < ns; const int rn = more ? CONV_RIDX(sq + 1) : r;
;             if (more) { CONV_DESC(rn, tn); titem_issue(tn, F.lane, scr + (p ^ 1) * 8192); }
;             if (!more) asm volatile("s_waitcnt vmcnt(0)" ::: "memory");
;             else if (first) asm volatile("s_waitcnt vmcnt(8)" ::: "memory");
;             else asm volatile("s_waitcnt vmcnt(12)" ::: "memory");
;             titem_finish(tc, F.lane, scr + p * 8192);
;             asm volatile("s_waitcnt lgkmcnt(0)" ::: "memory");
;             if (!more) break;
;             tc = tn; r = rn; ++sq; p ^= 1; first = false;
;         }
;     }
;     ...
;     __syncthreads();
.Lcv1_goC6:
	s_mov_b32 s65, s64
	v_mad_u32_u24 v6, v2, s9, v4
	global_load_dwordx4 v[164:167], v6, s[4:5] nt
	s_add_u32 s4, s4, s8
	s_addc_u32 s5, s5, 0
	global_load_dwordx4 v[168:171], v6, s[4:5] nt
	s_add_u32 s4, s4, s8
	s_addc_u32 s5, s5, 0
	global_load_dwordx4 v[172:175], v6, s[4:5] nt
	s_add_u32 s4, s4, s8
	s_addc_u32 s5, s5, 0
	global_load_dwordx4 v[176:179], v6, s[4:5] nt
	s_add_u32 s4, s4, s8
	s_addc_u32 s5, s5, 0
	global_load_dwordx4 v[180:183], v6, s[4:5] nt
	s_add_u32 s4, s4, s8
	s_addc_u32 s5, s5, 0
	global_load_dwordx4 v[184:187], v6, s[4:5] nt
	s_add_u32 s4, s4, s8
	s_addc_u32 s5, s5, 0
	global_load_dwordx4 v[188:191], v6, s[4:5] nt
	s_add_u32 s4, s4, s8
	s_addc_u32 s5, s5, 0
	global_load_dwordx4 v[192:195], v6, s[4:5] nt
	s_add_u32 s4, s4, s8
	s_addc_u32 s5, s5, 0
	global_load_dwordx4 v[196:199], v6, s[4:5] nt
	s_add_u32 s4, s4, s8
	s_addc_u32 s5, s5, 0
	global_load_dwordx4 v[200:203], v6, s[4:5] nt
	s_add_u32 s4, s4, s8
	s_addc_u32 s5, s5, 0
	global_load_dwordx4 v[204:207], v6, s[4:5] nt
	s_add_u32 s4, s4, s8
	s_addc_u32 s5, s5, 0
	global_load_dwordx4 v[208:211], v6, s[4:5] nt
	s_add_u32 s4, s4, s8
	s_addc_u32 s5, s5, 0
	global_load_dwordx4 v[212:215], v6, s[4:5] nt
	s_add_u32 s4, s4, s8
	s_addc_u32 s5, s5, 0
	global_load_dwordx4 v[216:219], v6, s[4:5] nt
	s_add_u32 s4, s4, s8
	s_addc_u32 s5, s5, 0
	global_load_dwordx4 v[220:223], v6, s[4:5] nt
	s_add_u32 s4, s4, s8
	s_addc_u32 s5, s5, 0
	global_load_dwordx4 v[224:227], v6, s[4:5] nt
	s_add_u32 s69, s69, s71
	s_branch .Lcv1_loop
.Lcv1_done:
.LBB0_186:
	s_waitcnt vmcnt(0)
	s_barrier

; #define LAS __attribute__((address_space(3)))
; __device__ __forceinline__ void convert_experts(Frame& F, int lo, int hi) {
;     const int gw = F.vcu * 8 + F.wave, NGW = F.G * 8;
;     LAS unsigned char* scr = F.lds + F.wave * 16384;
; __global__ void __launch_bounds__(NTHR, 2) hybrid_fwd(Args args) {
;     ...
;         if (!conv_first && rep == 0) { Frame F = make_frame(lds); convert_experts(F, 0, CONV_ITEMS); }
.LBB0_203:
	s_andn2_b64 vcc, exec, s[20:21]
	s_cbranch_vccnz .LBB0_248
	s_load_dword s8, s[0:1], 0xd0
	s_load_dwordx8 s[72:79], s[0:1], 0x80
	s_load_dwordx4 s[80:83], s[0:1], 0xa0
	s_load_dwordx2 s[84:85], s[0:1], 0xc0
	v_and_b32_e32 v1, 63, v0
	v_lshrrev_b32_e32 v2, 3, v1
	v_and_b32_e32 v3, 7, v1
	v_lshlrev_b32_e32 v4, 4, v3
	v_lshlrev_b32_e32 v5, 4, v2
	v_readfirstlane_b32 s9, v0
	s_waitcnt lgkmcnt(0)
	s_lshr_b32 s9, s9, 6
	s_and_b32 s10, s8, 7
	s_mov_b32 s11, s2
	s_cmp_lg_u32 s10, 0
	s_cbranch_scc1 .Lcv2_vcu
	s_and_b32 s10, s2, 7
	s_lshr_b32 s11, s8, 3
	s_mul_i32 s11, s11, s10
	s_lshr_b32 s10, s2, 3
	s_add_u32 s11, s11, s10

; #define LAS __attribute__((address_space(3)))
; __device__ __forceinline__ void phase_attn(Frame& F) {
;     const bf16_t* qkv = WSP(F, WS_B, bf16_t);
;     bf16_t* part = (bf16_t*)F.a->out;
;     float* lse = WSP(F, WS_LSE, float);
;     const int tid = F.tid, w = F.wave, lane = F.lane, fr = lane & 15, fq = lane >> 4;
;     const int x8 = blockIdx.x & 7, r8 = blockIdx.x >> 3, G8 = F.G >> 3;
;     constexpr int PER_X = 16 * 96;
;     constexpr int ABUF = 2 * ATT_VOFF;
;     float ef[4];
; #pragma unroll
;     for (int rg = 0; rg < 4; ++rg) ef[rg] = (float)(fr - 4 * fq - rg);
;     const int ql = 16 * w + fr;
;     u32x4 kr[4], vr[4];
;     AttnUnit un;
;     bf16x8 qn0, qn1;
;     int jl = r8;
;     if (jl >= PER_X) return;
;     AttnUnit cu = attn_decode(x8 * PER_X + jl);
;     attn_issue(qkv, cu, tid, kr, vr);
;     { const char* qb = (const char*)qkv + (((size_t)cu.b * SEQ + cu.r) * NPROJ + cu.h * 64) * 2; const unsigned qo = __umul24((unsigned)(128 * cu.n + ql), (unsigned)cu.d * (NPROJ * 2)) + 16u * fq;
;       qn0 = *(const bf16x8*)(qb + qo); qn1 = *(const bf16x8*)(qb + qo + 64); }
; #pragma unroll
;     for (int jj = 0; jj < 4; ++jj) { const int ch = tid + 512 * jj, row = ch >> 3, c16 = ch & 7;
;         *(LAS u32x4*)(F.lds + row * ATT_ROWB + c16 * 16) = kr[jj]; *(LAS u32x4*)(F.lds + ATT_VOFF + row * ATT_ROWB + c16 * 16) = vr[jj]; }
;     const int jlast = r8 + G8 * ((PER_X - 1 - r8) / G8);
;     un = attn_decode(x8 * PER_X + (jl + G8 < jlast ? jl + G8 : jlast)); attn_issue(qkv, un, tid, kr, vr);
.LBB0_300:
	s_cmp_lt_i32 s62, 4
	s_cselect_b64 s[6:7], -1, 0
	s_and_b64 s[22:23], s[6:7], s[4:5]
	s_andn2_b64 vcc, exec, s[22:23]
	s_cbranch_vccnz .LBB0_313
	s_add_u32 s28, s0, 0xd0
	s_addc_u32 s29, s1, 0
	v_mov_b32_e32 v42, v0
	s_cmpk_gt_u32 s2, 0x2fff
	s_mov_b64 s[4:5], s[0:1]
	v_readfirstlane_b32 s3, v42
	s_cbranch_scc1 .LBB0_307
	s_load_dwordx4 s[24:27], s[4:5], 0xb8
	s_and_b32 s4, s2, 7
	s_ashr_i32 s14, s3, 6
	s_load_dword s5, s[28:29], 0x0
	s_mul_i32 s3, s4, 0x600
	s_waitcnt lgkmcnt(0)
	s_add_u32 s33, s26, 0x151c0000
	s_addc_u32 s66, s27, 0
	s_add_u32 s67, s26, 0x291c0000
	s_addc_u32 s68, s27, 0
	s_lshr_b32 s70, s2, 3
	s_add_i32 s4, s3, s70
	s_mul_i32 s9, s4, 0xaaab
	s_ashr_i32 s69, s5, 3
	s_lshr_b32 s5, s9, 22
	s_mulk_i32 s5, 0x60
	s_sub_i32 s4, s4, s5
	s_lshl_b32 s56, s14, 4
	s_sub_i32 s8, 0x5ff, s70
	s_and_b32 s10, s4, 0xffff
	s_cmp_gt_u32 s10, 31
	s_cselect_b64 s[4:5], -1, 0
	s_cmp_gt_u32 s10, 63
	s_cselect_b64 s[6:7], -1, 0
	v_cndmask_b32_e64 v1, 0, 1, s[6:7]
	s_cmp_lg_u64 s[4:5], 0
	v_readfirstlane_b32 s6, v1
	s_addc_u32 s26, s6, 0
	s_lshl_b32 s4, s26, 5
	s_lshl_b32 s35, s26, 1
	s_sub_i32 s6, s10, s4
	s_sub_i32 s7, 5, s35
	s_lshr_b32 s34, s9, 25
	s_ashr_i32 s31, s6, s7
	s_lshl_b32 s4, s34, 12
	s_add_i32 s4, s31, s4
	s_bfe_u32 s30, s9, 0x30016
	s_mul_hi_i32 s5, s4, 0xa00
	s_mulk_i32 s4, 0xa00
	s_lshl_b32 s9, s30, 6
	s_lshl_b32 s7, -1, s7
	s_or_b32 s4, s4, s9
	s_andn2_b32 s64, s6, s7
	v_ashrrev_i32_e32 v1, 3, v42
	s_lshl_b64 s[4:5], s[4:5], 1
	s_lshl_b32 s9, s64, 7
	s_lshl_b32 s10, 0x1400, s35
	v_add_u32_e32 v81, 0xffffff80, v1
	s_add_u32 s4, s33, s4
	v_add_u32_e32 v2, s9, v81
	s_addc_u32 s5, s66, s5
	v_lshlrev_b32_e32 v43, 4, v42
	v_max_i32_e32 v3, 0, v2
	s_add_u32 s6, s4, 0x400
	v_and_b32_e32 v80, 0x70, v43
	v_mul_u32_u24_e32 v3, s10, v3
	s_addc_u32 s7, s5, 0
	v_or_b32_e32 v3, v3, v80
	global_load_dwordx4 v[10:13], v3, s[6:7]
	global_load_dwordx4 v[14:17], v3, s[6:7] offset:1024
	v_max_i32_e32 v3, 0xffffffc0, v2
	v_add_u32_e32 v3, 64, v3
	v_mul_u32_u24_e32 v3, s10, v3
	v_or_b32_e32 v3, v3, v80
	global_load_dwordx4 v[18:21], v3, s[6:7]
	global_load_dwordx4 v[22:25], v3, s[6:7] offset:1024
	v_add_u32_e32 v3, s9, v1
	v_max_i32_e32 v3, 0, v3
	v_mul_u32_u24_e32 v3, s10, v3
	v_or_b32_e32 v3, v3, v80
	global_load_dwordx4 v[26:29], v3, s[6:7]
	global_load_dwordx4 v[30:33], v3, s[6:7] offset:1024
	v_max_i32_e32 v2, 0xffffff40, v2
	v_add_u32_e32 v2, 0xc0, v2
	v_mul_u32_u24_e32 v2, s10, v2
	v_or_b32_e32 v2, v2, v80
	global_load_dwordx4 v[34:37], v2, s[6:7]
	global_load_dwordx4 v[38:41], v2, s[6:7] offset:1024
	v_and_b32_e32 v45, 15, v42
	v_bfe_u32 v2, v42, 2, 4
	v_and_b32_e32 v47, 12, v2
	v_or_b32_e32 v2, 3, v2
	v_or_b32_e32 v86, s56, v45
	v_sub_u32_e32 v54, v45, v2
	v_add_u32_e32 v2, s9, v86
	v_and_b32_e32 v82, 48, v42
	s_movk_i32 s58, 0x90
	v_add_u32_e32 v3, 0x200, v42
	v_mul_u32_u24_e32 v2, s10, v2
	v_mul_lo_u32 v83, v1, s58
	v_lshrrev_b32_e32 v3, 3, v3
	v_or_b32_e32 v4, 2, v47
	v_add_u32_e32 v84, 0, v80
	v_or_b32_e32 v58, v2, v82
	v_mul_lo_u32 v85, v3, s58
	v_sub_u32_e32 v55, v45, v4
	v_add_u32_e32 v56, v84, v83
	global_load_dwordx4 v[2:5], v58, s[4:5]
	global_load_dwordx4 v[6:9], v58, s[4:5] offset:64
	s_abs_i32 s4, s69
	v_add_u32_e32 v57, v84, v85
	s_sub_i32 s5, 0, s4
	v_add_u32_e32 v46, 0x400, v42
	v_and_b32_e32 v89, 48, v43
	v_and_b32_e32 v44, 63, v42
	v_sub_u32_e32 v48, v45, v47
	v_xad_u32 v49, v47, -1, v45
	v_cvt_f32_i32_e32 v50, v48
	v_cvt_f32_i32_e32 v51, v49
	v_cvt_f32_i32_e32 v53, v54
	v_cvt_f32_i32_e32 v52, v55
	s_mov_b32 s27, 0
	v_mul_lo_u32 v90, v86, s58
	v_cmp_gt_i32_e64 s[12:13], 1, v54
	v_cmp_lt_i32_e64 s[16:17], -1, v49
	v_cmp_lt_i32_e64 s[18:19], -1, v55
	v_cmp_lt_i32_e64 s[20:21], -1, v54
	v_mov_b32_e32 v109, 0xff800000
	s_waitcnt vmcnt(0)
	ds_write_b128 v56, v[10:13]
	ds_write_b128 v56, v[14:17] offset:36864
	ds_write_b128 v57, v[18:21]
	ds_write_b128 v57, v[22:25] offset:36864
	v_cvt_f32_u32_e32 v11, s4
	v_lshrrev_b32_e32 v10, 3, v46
	v_mul_lo_u32 v87, v10, s58
	v_add_u32_e32 v10, v84, v87
	v_rcp_iflag_f32_e32 v11, v11
	ds_write_b128 v10, v[26:29]
	ds_write_b128 v10, v[30:33] offset:36864
	v_add_u32_e32 v10, 0x600, v42
	v_lshrrev_b32_e32 v10, 3, v10
	v_mul_f32_e32 v11, 0x4f7ffffe, v11
	v_cvt_u32_f32_e32 v11, v11
	v_mul_lo_u32 v88, v10, s58
	v_add_u32_e32 v10, v84, v88
	ds_write_b128 v10, v[34:37]
	ds_write_b128 v10, v[38:41] offset:36864
	v_readfirstlane_b32 s6, v11
	s_mul_i32 s5, s5, s6
	s_mul_hi_u32 s5, s6, s5
	s_add_i32 s6, s6, s5
	s_mul_hi_u32 s5, s8, s6
	s_mul_i32 s5, s5, s4
	s_sub_i32 s5, s8, s5
	s_sub_i32 s6, s5, s4
	s_cmp_ge_u32 s5, s4
	s_cselect_b32 s5, s6, s5
	s_sub_i32 s6, s5, s4
	s_cmp_ge_u32 s5, s4
	s_cselect_b32 s4, s6, s5
	s_sub_i32 s71, s8, s4
	s_add_i32 s71, s71, s70
	s_add_i32 s4, s69, s70
	s_min_i32 s4, s4, s71
	s_add_i32 s6, s4, s3
	s_mul_hi_i32 s4, s6, 0x2aaaaaab
	s_lshr_b32 s5, s4, 31
	s_ashr_i32 s4, s4, 4
	s_add_i32 s10, s4, s5
	s_ashr_i32 s36, s10, 3
	s_ashr_i32 s37, s36, 31
	s_mul_i32 s7, s10, 0x60
	s_lshl_b64 s[4:5], s[36:37], 12
	s_sub_i32 s11, s6, s7
	s_cmp_gt_i32 s11, 31
	s_cselect_b64 s[6:7], -1, 0
	s_cmp_gt_i32 s11, 63
	s_cselect_b64 s[8:9], -1, 0
	v_cndmask_b32_e64 v10, 0, 1, s[8:9]
	s_cmp_lg_u64 s[6:7], 0
	v_readfirstlane_b32 s8, v10
	s_addc_u32 s72, s8, 0
	s_lshl_b32 s6, s72, 5
	s_lshl_b32 s74, s72, 1
	s_sub_i32 s6, s11, s6
	s_sub_i32 s7, 5, s74
	s_ashr_i32 s73, s6, s7
	s_ashr_i32 s8, s73, 31
	s_add_u32 s4, s4, s73
	s_addc_u32 s5, s5, s8
	s_mulk_i32 s5, 0xa00
	s_mul_hi_u32 s8, s4, 0xa00
	s_and_b32 s75, s10, 7
	s_add_i32 s5, s8, s5
	s_mulk_i32 s4, 0xa00
	s_lshl_b32 s8, s75, 6
	s_or_b32 s4, s4, s8
	s_lshl_b64 s[4:5], s[4:5], 1
	s_add_u32 s4, s33, s4
	s_addc_u32 s5, s66, s5
; #define LAS __attribute__((address_space(3)))
; __device__ __forceinline__ void convert_experts(Frame& F, int lo, int hi) {
;     const int gw = F.vcu * 8 + F.wave, NGW = F.G * 8;
;     LAS unsigned char* scr = F.lds + F.wave * 16384;
;     unsigned char* W1t = WSP(F, WS_W1T, unsigned char); unsigned char* W2t = WSP(F, WS_W2T, unsigned char);
;     const float* weg = F.a->in[I_WEG]; const float* weu = F.a->in[I_WEU]; const float* wed = F.a->in[I_WED];
;     const float* wsg = F.a->in[I_WSG]; const float* wsu = F.a->in[I_WSU]; const float* wsd = F.a->in[I_WSD];
; __device__ __forceinline__ void phase_attn(Frame& F) {
;     ...
;     un = attn_decode(x8 * PER_X + (jl + G8 < jlast ? jl + G8 : jlast)); attn_issue(qkv, un, tid, kr, vr);
;     int buf = 0;
;     for (; jl < PER_X; jl += G8) {
;         lds_barrier();
;         LAS unsigned char* kb = F.lds + buf * ABUF;
;         const bf16x8 q0 = qn0, q1 = qn1;
;         {
;             LAS unsigned char* ob = F.lds + (buf ^ 1) * ABUF;
; #pragma unroll
;             for (int jj = 0; jj < 4; ++jj) { const int ch = tid + 512 * jj, row = ch >> 3, c16 = ch & 7;
;                 *(LAS u32x4*)(ob + row * ATT_ROWB + c16 * 16) = kr[jj]; *(LAS u32x4*)(ob + ATT_VOFF + row * ATT_ROWB + c16 * 16) = vr[jj]; }
;         }
;         const AttnUnit nu = un;
;         un = attn_decode(x8 * PER_X + (jl + 2 * G8 < jlast ? jl + 2 * G8 : jlast)); attn_issue(qkv, un, tid, kr, vr);
;         { const char* qb = (const char*)qkv + (((size_t)nu.b * SEQ + nu.r) * NPROJ + nu.h * 64) * 2; const unsigned qo = __umul24((unsigned)(128 * nu.n + ql), (unsigned)nu.d * (NPROJ * 2)) + 16u * fq;
;           qn0 = *(const bf16x8*)(qb + qo); qn1 = *(const bf16x8*)(qb + qo + 64); }
;         const unsigned qrow = __umul24((unsigned)(128 * cu.n + ql), (unsigned)cu.d);
;         const float c1 = 0.125f * LOG2E;
;         const float nc2 = -__builtin_amdgcn_exp2f(-(float)(cu.h + 1)) * (float)cu.d * LOG2E;
;         const bool first = cu.n == 0;
;         f32x4 St[9];
;         const f32x4 eb = (f32x4){ef[0], ef[1], ef[2], ef[3]} * nc2;
;         float mx = -INFINITY;
;         bf16x8 kf[9][2];
; #pragma unroll
;         for (int T = 0; T < 9; ++T) { LAS unsigned char* ka = kb + (16 * (w + T) + fr) * ATT_ROWB + fq * 16; kf[T][0] = *(LAS bf16x8*)ka; kf[T][1] = *(LAS bf16x8*)(ka + 64); }
	s_add_u32 s4, s4, 0x400
	s_addc_u32 s5, s5, 0
	s_lshl_b32 s7, -1, s7
	s_andn2_b32 s76, s6, s7
	s_lshl_b32 s6, s76, 7
	v_add_u32_e32 v34, s6, v81
	v_max_i32_e32 v10, 0xffffff40, v34
	v_add_u32_e32 v10, 0xc0, v10
	s_lshl_b32 s7, 0x1400, s74
	v_mul_u32_u24_e32 v10, s7, v10
	v_or_b32_e32 v18, v10, v80
	global_load_dwordx4 v[10:13], v18, s[4:5] offset:1024
	global_load_dwordx4 v[14:17], v18, s[4:5]
	v_add_u32_e32 v18, s6, v1
	v_max_i32_e32 v18, 0, v18
	v_mul_u32_u24_e32 v18, s7, v18
	v_or_b32_e32 v26, v18, v80
	global_load_dwordx4 v[18:21], v26, s[4:5] offset:1024
	global_load_dwordx4 v[22:25], v26, s[4:5]
	v_max_i32_e32 v26, 0xffffffc0, v34
	v_add_u32_e32 v26, 64, v26
	v_max_i32_e32 v34, 0, v34
	v_mul_u32_u24_e32 v26, s7, v26
	v_mul_u32_u24_e32 v34, s7, v34
	v_or_b32_e32 v35, v26, v80
	v_or_b32_e32 v46, v34, v80
	global_load_dwordx4 v[26:29], v35, s[4:5] offset:1024
	global_load_dwordx4 v[30:33], v35, s[4:5]
	s_nop 0
	global_load_dwordx4 v[34:37], v46, s[4:5] offset:1024
	global_load_dwordx4 v[38:41], v46, s[4:5]
	s_add_i32 s37, s56, 16
	v_or_b32_e32 v43, s37, v45
	s_add_i32 s59, s56, 32
	v_mul_lo_u32 v91, v43, s58
	v_or_b32_e32 v43, s59, v45
	s_add_i32 s65, s56, 48
	v_mul_lo_u32 v92, v43, s58
	v_or_b32_e32 v43, s65, v45
	s_add_i32 s78, s56, 64
	v_mul_lo_u32 v93, v43, s58
	v_or_b32_e32 v43, s78, v45
	s_add_i32 s79, s56, 0x50
	v_mul_lo_u32 v94, v43, s58
	v_or_b32_e32 v43, s79, v45
	s_add_i32 s80, s56, 0x60
	v_mul_lo_u32 v95, v43, s58
	v_or_b32_e32 v43, s80, v45
	s_add_i32 s81, s56, 0x70
	v_bfe_u32 v42, v42, 2, 2
	v_mul_lo_u32 v96, v43, s58
	v_or_b32_e32 v43, s81, v45
	s_add_i32 s82, s56, 0x80
	s_lshl_b32 s77, s69, 1
	v_or_b32_e32 v42, v47, v42
	v_mul_lo_u32 v97, v43, s58
	v_or_b32_e32 v43, s82, v45
	v_mul_lo_u32 v98, v43, s58
	s_cmp_gt_i32 s14, 7
	v_or_b32_e32 v43, s56, v42
	s_cselect_b64 s[38:39], -1, 0
	s_cmp_gt_i32 s14, 6
	v_mul_lo_u32 v99, v43, s58
	v_or_b32_e32 v43, s37, v42
	s_cselect_b64 s[40:41], -1, 0
	s_cmp_gt_i32 s14, 5
	v_mul_lo_u32 v100, v43, s58
	v_or_b32_e32 v43, s59, v42
	s_cselect_b64 s[42:43], -1, 0
	s_cmp_gt_i32 s14, 4
	v_mul_lo_u32 v101, v43, s58
	v_or_b32_e32 v43, s65, v42
	s_cselect_b64 s[44:45], -1, 0
	s_cmp_gt_i32 s14, 3
	v_mul_lo_u32 v102, v43, s58
	v_or_b32_e32 v43, s78, v42
	s_cselect_b64 s[46:47], -1, 0
	s_cmp_gt_i32 s14, 2
	v_mul_lo_u32 v103, v43, s58
	v_or_b32_e32 v43, s79, v42
	s_cselect_b64 s[48:49], -1, 0
	s_cmp_gt_i32 s14, 1
	v_mul_lo_u32 v104, v43, s58
	v_or_b32_e32 v43, s80, v42
	s_cselect_b64 s[50:51], -1, 0
	s_cmp_gt_i32 s14, 0
	v_mul_lo_u32 v105, v43, s58
	v_or_b32_e32 v43, s81, v42
	v_or_b32_e32 v42, s82, v42
	s_cselect_b64 s[52:53], -1, 0
	s_cmp_gt_i32 s14, -1
	v_mul_lo_u32 v107, v42, s58
	v_mbcnt_lo_u32_b32 v42, -1, 0
	v_cmp_gt_u32_e64 s[4:5], 16, v44
	v_cmp_gt_i32_e64 s[6:7], 1, v48
	v_cmp_gt_i32_e64 s[8:9], 1, v49
	v_cmp_gt_i32_e64 s[10:11], 1, v55
	s_cselect_b64 s[54:55], -1, 0
	v_cmp_lt_i32_e64 s[14:15], -1, v48
	v_mul_lo_u32 v106, v43, s58
	s_mov_b32 s78, 0xff800000
	s_mov_b32 s56, 0x3e38aa3b
	v_mbcnt_hi_u32_b32 v108, -1, v42
	s_mov_b32 s79, 0
	s_load_dwordx8 s[92:99], s[0:1], 0x80
	s_waitcnt lgkmcnt(0)
	v_writelane_b32 v253, s92, 0
	v_writelane_b32 v253, s93, 1
	v_writelane_b32 v253, s94, 2
	v_writelane_b32 v253, s95, 3
	v_writelane_b32 v253, s96, 4
	v_writelane_b32 v253, s97, 5
	v_writelane_b32 v253, s98, 6
	v_writelane_b32 v253, s99, 7
	s_load_dwordx4 s[92:95], s[0:1], 0xa0
	s_load_dwordx2 s[96:97], s[0:1], 0xc0
	s_load_dword s98, s[0:1], 0xd0
	s_waitcnt lgkmcnt(0)
	v_writelane_b32 v253, s92, 8
	v_writelane_b32 v253, s93, 9
	v_writelane_b32 v253, s94, 10
	v_writelane_b32 v253, s95, 11
	s_add_u32 s92, s96, 0x1100000
	s_addc_u32 s93, s97, 0
	s_add_u32 s94, s96, 0x9180000
	s_addc_u32 s95, s97, 0
	v_writelane_b32 v253, s92, 12
	v_writelane_b32 v253, s93, 13
	v_writelane_b32 v253, s94, 14
	v_writelane_b32 v253, s95, 15
	v_and_b32_e32 v248, 63, v0
	v_and_b32_e32 v249, 7, v248
	v_lshlrev_b32_e32 v249, 4, v249
	v_lshrrev_b32_e32 v248, 3, v248
	v_readfirstlane_b32 s99, v0
	s_and_b32 s100, s98, 7
	s_mov_b32 s101, s2
	s_cmp_lg_u32 s100, 0
	s_cbranch_scc1 .Lcva_vcu
	s_and_b32 s100, s2, 7
	s_lshr_b32 s101, s98, 3
	s_mul_i32 s101, s101, s100
	s_lshr_b32 s100, s2, 3
	s_add_u32 s101, s101, s100
; #define LAS __attribute__((address_space(3)))
; __device__ __forceinline__ void titem_issue(const TItem& t, int lane, LAS unsigned char* buf) {
;     const int nblk = t.N / 32, kb = t.item / nblk, nb = t.item % nblk, k0 = 64 * kb, n0 = 32 * nb;
; #pragma unroll
;     for (int j = 0; j < 8; ++j) { const float* g = t.W + (size_t)(k0 + 8 * j + (lane >> 3)) * t.N + n0 + 4 * ((lane & 7) ^ j);
;         __builtin_amdgcn_global_load_lds((const unsigned*)g, (LAS unsigned*)(buf + j * 1024), 16, 0, 2); }
; }
; __device__ __forceinline__ void convert_experts(Frame& F, int lo, int hi) {
;     ...
;     constexpr int NPAIRS = CONV_ITEMS / 2;
;     (void)lo; (void)hi;
;     ...
;     if (gw < NPAIRS) {
;         const int ns = 2 * ((NPAIRS - gw + NGW - 1) / NGW);
;         int sq = 0, r = CONV_RIDX(0);
;         TItem tc, tn; CONV_DESC(r, tc); tn = tc;
;         int p = 0; bool first = true;
;         titem_issue(tc, F.lane, scr);
;         for (;;) {
;             const bool more = sq + 1 < ns; const int rn = more ? CONV_RIDX(sq + 1) : r;
;             if (more) { CONV_DESC(rn, tn); titem_issue(tn, F.lane, scr + (p ^ 1) * 8192); }
;             if (!more) asm volatile("s_waitcnt vmcnt(0)" ::: "memory");
;             else if (first) asm volatile("s_waitcnt vmcnt(8)" ::: "memory");
.Lcva_vcu:
	s_lshr_b32 s99, s99, 6
	s_lshl_b32 s101, s101, 3
	s_add_u32 s89, s101, s99
	s_movk_i32 s90, 12
	s_and_b32 s32, s89, 3
	s_mov_b32 s95, 0
	s_and_b32 s98, s32, 3
	s_add_u32 s32, s32, 1
	s_cmp_eq_u32 s98, 0
	s_cbranch_scc0 .Lcva_dummy_pre
	s_cmp_eq_u32 s90, 0
	s_cbranch_scc1 .Lcva_dummy_pre
	s_sub_u32 s90, s90, 1
	s_lshr_b32 s98, s89, 6
	s_and_b32 s99, s89, 63
	s_mul_hi_u32 s100, s98, 0xaaaaaaab
	s_lshr_b32 s100, s100, 1
	s_mul_i32 s101, s100, 3
	s_sub_u32 s101, s98, s101
	s_cmp_lt_u32 s100, 256
	s_cselect_b32 s98, 0, 3
	s_cselect_b32 s95, s100, 0
	s_add_u32 s98, s98, s101
	s_lshl_b32 s98, s98, 1
	v_readlane_b32 s96, v253, s98
	s_add_u32 s98, s98, 1
	v_readlane_b32 s97, v253, s98
	s_lshl_b32 s95, s95, 20
	s_nop 3
	s_add_u32 s96, s96, s95
	s_addc_u32 s97, s97, 0
	s_cmp_eq_u32 s101, 2
	s_cbranch_scc1 .Lcva_down_pre
	s_lshr_b32 s95, s99, 3
	s_and_b32 s99, s99, 7
	s_lshl_b32 s98, s95, 17
	s_add_u32 s96, s96, s98
	s_addc_u32 s97, s97, 0
	s_lshl_b32 s98, s99, 7
	s_add_u32 s96, s96, s98
	s_addc_u32 s97, s97, 0
	s_lshl_b32 s100, s100, 19
	s_lshr_b32 s98, s99, 2
	s_lshl_b32 s98, s98, 18
	s_add_u32 s100, s100, s98
	s_and_b32 s98, s99, 3
	s_lshl_b32 s98, s98, 15
	s_add_u32 s100, s100, s98
	s_lshl_b32 s98, s101, 17
	s_add_u32 s100, s100, s98
	s_lshl_b32 s98, s95, 7
	s_add_u32 s100, s100, s98
	v_readlane_b32 s92, v253, 12
	v_readlane_b32 s93, v253, 13
	s_mov_b32 s94, 0xc3317218
	s_cmp_eq_u32 s101, 0
	s_cselect_b32 s94, 0xc2b8aa3b, s94
	s_nop 3
	s_add_u32 s92, s92, s100
	s_addc_u32 s93, s93, 0
	s_movk_i32 s95, 0x400
	s_movk_i32 s98, 0x400
	s_branch .Lcva_go_pre
.Lcva_down_pre:
	s_lshr_b32 s95, s99, 5
	s_and_b32 s99, s99, 31
	s_lshl_b32 s98, s95, 19
	s_add_u32 s96, s96, s98
	s_addc_u32 s97, s97, 0
	s_lshl_b32 s98, s99, 7
	s_add_u32 s96, s96, s98
	s_addc_u32 s97, s97, 0
	s_lshl_b32 s100, s100, 18
	s_lshl_b32 s98, s99, 13
	s_add_u32 s100, s100, s98
	s_lshl_b32 s98, s95, 7
	s_add_u32 s100, s100, s98
	v_readlane_b32 s92, v253, 14
	v_readlane_b32 s93, v253, 15
	s_mov_b32 s94, 0x42800000
	s_nop 3
	s_add_u32 s92, s92, s100
	s_addc_u32 s93, s93, 0
	s_movk_i32 s95, 0x100
	s_movk_i32 s98, 0x1000
	s_branch .Lcva_go_pre
.Lcva_dummy_pre:
	v_readlane_b32 s96, v253, 0
	v_readlane_b32 s97, v253, 1
	s_and_b32 s98, s89, 0x7ff
	s_lshl_b32 s98, s98, 7
	s_mov_b32 s95, 0
	s_nop 1
	s_add_u32 s96, s96, s98
	s_addc_u32 s97, s97, 0
	s_mov_b32 s98, 0
.Lcva_go_pre:
	s_lshl_b32 s99, s98, 4
	v_mad_u32_u24 v250, v248, s99, v249
	global_load_dwordx4 v[168:171], v250, s[96:97] nt
	s_add_u32 s96, s96, s98
	s_addc_u32 s97, s97, 0
	global_load_dwordx4 v[172:175], v250, s[96:97] nt
	s_add_u32 s96, s96, s98
	s_addc_u32 s97, s97, 0
	global_load_dwordx4 v[176:179], v250, s[96:97] nt
	s_add_u32 s96, s96, s98
	s_addc_u32 s97, s97, 0
	global_load_dwordx4 v[180:183], v250, s[96:97] nt
	s_add_u32 s96, s96, s98
	s_addc_u32 s97, s97, 0
	global_load_dwordx4 v[184:187], v250, s[96:97] nt
	s_add_u32 s96, s96, s98
	s_addc_u32 s97, s97, 0
	global_load_dwordx4 v[188:191], v250, s[96:97] nt
	s_add_u32 s96, s96, s98
	s_addc_u32 s97, s97, 0
	global_load_dwordx4 v[192:195], v250, s[96:97] nt
	s_add_u32 s96, s96, s98
	s_addc_u32 s97, s97, 0
	global_load_dwordx4 v[196:199], v250, s[96:97] nt
	s_add_u32 s96, s96, s98
	s_addc_u32 s97, s97, 0
	global_load_dwordx4 v[200:203], v250, s[96:97] nt
	s_add_u32 s96, s96, s98
	s_addc_u32 s97, s97, 0
	global_load_dwordx4 v[204:207], v250, s[96:97] nt
	s_add_u32 s96, s96, s98
	s_addc_u32 s97, s97, 0
	global_load_dwordx4 v[208:211], v250, s[96:97] nt
	s_add_u32 s96, s96, s98
	s_addc_u32 s97, s97, 0
	global_load_dwordx4 v[212:215], v250, s[96:97] nt
	s_add_u32 s96, s96, s98
	s_addc_u32 s97, s97, 0
	global_load_dwordx4 v[216:219], v250, s[96:97] nt
	s_add_u32 s96, s96, s98
	s_addc_u32 s97, s97, 0
	global_load_dwordx4 v[220:223], v250, s[96:97] nt
	s_add_u32 s96, s96, s98
	s_addc_u32 s97, s97, 0
	global_load_dwordx4 v[224:227], v250, s[96:97] nt
	s_add_u32 s96, s96, s98
	s_addc_u32 s97, s97, 0
	global_load_dwordx4 v[228:231], v250, s[96:97] nt
	s_lshl_b32 s99, s69, 6
	s_cmp_eq_u32 s95, 0
	s_cselect_b32 s99, 0, s99
	s_add_u32 s89, s89, s99
	s_waitcnt vmcnt(0)
	s_branch .LBB0_304

; #define LAS __attribute__((address_space(3)))
; __device__ __forceinline__ void phase_attn(Frame& F) {
;     ...
;         const unsigned qrow = __umul24((unsigned)(128 * cu.n + ql), (unsigned)cu.d);
;         const float c1 = 0.125f * LOG2E;
;         const float nc2 = -__builtin_amdgcn_exp2f(-(float)(cu.h + 1)) * (float)cu.d * LOG2E;
;         const bool first = cu.n == 0;
;         f32x4 St[9];
;         const f32x4 eb = (f32x4){ef[0], ef[1], ef[2], ef[3]} * nc2;
;         float mx = -INFINITY;
;         bf16x8 kf[9][2];
; #pragma unroll
;         for (int T = 0; T < 9; ++T) { LAS unsigned char* ka = kb + (16 * (w + T) + fr) * ATT_ROWB + fq * 16; kf[T][0] = *(LAS bf16x8*)ka; kf[T][1] = *(LAS bf16x8*)(ka + 64); }
;         __builtin_amdgcn_sched_barrier(0);
; #pragma unroll
;         for (int T = 0; T < 9; ++T) {
;             f32x4 sa = (f32x4){0.f, 0.f, 0.f, 0.f};
;             sa = __builtin_amdgcn_mfma_f32_16x16x32_bf16(kf[T][0], q0, sa, 0, 0, 0);
;             sa = __builtin_amdgcn_mfma_f32_16x16x32_bf16(kf[T][1], q1, sa, 0, 0, 0);
;             const float kT = (!first || w + T >= 8) ? nc2 * (float)(128 - 16 * T) : -INFINITY;
;             sa = sa * c1 + (eb + kT);
; #pragma unroll
;             for (int rg = 0; rg < 4; ++rg) {
;                 if (T == 0) sa[rg] = ef[rg] <= 0.f ? sa[rg] : -INFINITY;
;                 if (T == 8) sa[rg] = ef[rg] >= 0.f ? sa[rg] : -INFINITY;
;             }
;             St[T] = sa;
;             mx = fmaxf(mx, fmaxf(fmaxf(sa[0], sa[1]), fmaxf(sa[2], sa[3])));
.LBB0_304:
	s_mul_i32 s37, s79, 0x12000
	s_add_i32 s85, s37, 0
	s_waitcnt vmcnt(19)
	v_mov_b64_e32 v[48:49], v[4:5]
	v_mov_b64_e32 v[46:47], v[2:3]
	v_mov_b64_e32 v[44:45], v[8:9]
	v_mov_b64_e32 v[42:43], v[6:7]
	s_lshl_b32 s65, 1, s35
	s_waitcnt lgkmcnt(0)
	s_barrier
	s_add_i32 s37, s30, 1
	v_cvt_f32_u32_e32 v54, s37
	v_cvt_f32_u32_e32 v55, s65
	v_add_u32_e32 v110, s85, v82
	v_add_u32_e32 v58, v110, v90
	v_exp_f32_e64 v54, -v54
	v_add_u32_e32 v66, v110, v91
	v_add_u32_e32 v74, v110, v92
	v_add_u32_e32 v111, v110, v93
	v_mul_f32_e32 v79, v55, v54
	ds_read_b128 v[54:57], v58
	ds_read_b128 v[58:61], v58 offset:64
	ds_read_b128 v[62:65], v66
	ds_read_b128 v[66:69], v66 offset:64
	ds_read_b128 v[70:73], v74
	ds_read_b128 v[74:77], v74 offset:64
	ds_read_b128 v[112:115], v111
	ds_read_b128 v[116:119], v111 offset:64
	v_add_u32_e32 v111, v110, v94
	ds_read_b128 v[120:123], v111
	ds_read_b128 v[124:127], v111 offset:64
	v_add_u32_e32 v111, v110, v95
	ds_read_b128 v[128:131], v111
	ds_read_b128 v[132:135], v111 offset:64
	v_add_u32_e32 v111, v110, v96
	ds_read_b128 v[136:139], v111
	ds_read_b128 v[140:143], v111 offset:64
	v_add_u32_e32 v111, v110, v97
	v_add_u32_e32 v110, v110, v98
	ds_read_b128 v[144:147], v111
	ds_read_b128 v[148:151], v111 offset:64
	ds_read_b128 v[152:155], v110
	ds_read_b128 v[156:159], v110 offset:64
	s_cmp_lg_u32 s64, 0
	v_lshl_add_u32 v78, s64, 7, v86
	s_cselect_b64 s[64:65], -1, 0
	v_mul_f32_e32 v160, 0xbfb8aa3b, v79
	v_and_b32_e32 v110, 0xffffff, v78
	s_waitcnt lgkmcnt(14)
	v_mfma_f32_16x16x32_bf16 v[54:57], v[54:57], v[46:49], 0
	v_mul_f32_e32 v78, 0x43000000, v160
	s_or_b64 vcc, s[64:65], s[38:39]
	v_cndmask_b32_e32 v78, v109, v78, vcc
	v_mfma_f32_16x16x32_bf16 v[54:57], v[58:61], v[42:45], v[54:57]
	v_fma_f32 v162, v50, v160, v78
	v_fma_f32 v163, v51, v160, v78
	v_pk_fma_f32 v[78:79], v[52:53], v[160:161], v[78:79] op_sel_hi:[1,0,0]
	s_or_b64 vcc, s[64:65], s[40:41]
	s_nop 3
	v_pk_fma_f32 v[56:57], v[56:57], s[56:57], v[78:79] op_sel_hi:[1,0,1]
	v_pk_fma_f32 v[54:55], v[54:55], s[56:57], v[162:163] op_sel_hi:[1,0,1]
	v_cndmask_b32_e64 v164, v109, v56, s[10:11]
	v_cndmask_b32_e64 v162, v109, v54, s[6:7]
	v_cndmask_b32_e64 v163, v109, v55, s[8:9]
	v_cndmask_b32_e64 v165, v109, v57, s[12:13]
	v_mfma_f32_16x16x32_bf16 v[54:57], v[62:65], v[46:49], 0
	v_max_f32_e32 v58, v162, v163
	v_max_f32_e32 v59, v164, v165
	v_max3_f32 v62, v58, v59, s78
	v_mfma_f32_16x16x32_bf16 v[54:57], v[66:69], v[42:45], v[54:57]
	v_mul_f32_e32 v58, 0x42e00000, v160
	v_cndmask_b32_e32 v58, v109, v58, vcc
	v_pk_fma_f32 v[60:61], v[50:51], v[160:161], v[58:59] op_sel_hi:[1,0,0]
	v_pk_fma_f32 v[58:59], v[52:53], v[160:161], v[58:59] op_sel_hi:[1,0,0]
	s_or_b64 vcc, s[64:65], s[42:43]
	s_nop 2
	v_pk_fma_f32 v[166:167], v[56:57], s[56:57], v[58:59] op_sel_hi:[1,0,1]
	s_waitcnt lgkmcnt(13)
	v_mfma_f32_16x16x32_bf16 v[56:59], v[70:73], v[46:49], 0
	v_fma_f32 v78, v54, s56, v60
	v_fma_f32 v79, v55, s56, v61
	v_max_f32_e32 v54, v166, v167
	v_max3_f32 v63, v78, v79, v54
	s_waitcnt lgkmcnt(12)
	v_mfma_f32_16x16x32_bf16 v[54:57], v[74:77], v[42:45], v[56:59]
	s_nop 2
	v_mul_f32_e32 v58, 0x42c00000, v160
	v_cndmask_b32_e32 v58, v109, v58, vcc
	v_pk_fma_f32 v[60:61], v[50:51], v[160:161], v[58:59] op_sel_hi:[1,0,0]
	v_pk_fma_f32 v[58:59], v[52:53], v[160:161], v[58:59] op_sel_hi:[1,0,0]
	s_nop 0
	v_pk_fma_f32 v[76:77], v[54:55], s[56:57], v[60:61] op_sel_hi:[1,0,1]
	v_pk_fma_f32 v[74:75], v[56:57], s[56:57], v[58:59] op_sel_hi:[1,0,1]
	s_waitcnt lgkmcnt(11)
	v_mfma_f32_16x16x32_bf16 v[54:57], v[112:115], v[46:49], 0
	v_max_f32_e32 v58, v74, v75
	v_max3_f32 v58, v76, v77, v58
	v_max3_f32 v62, v62, v63, v58
	s_waitcnt lgkmcnt(10)
	v_mfma_f32_16x16x32_bf16 v[54:57], v[116:119], v[42:45], v[54:57]
	v_mul_f32_e32 v58, 0x42a00000, v160
	s_or_b64 vcc, s[64:65], s[44:45]
	v_cndmask_b32_e32 v58, v109, v58, vcc
	v_pk_fma_f32 v[60:61], v[50:51], v[160:161], v[58:59] op_sel_hi:[1,0,0]
	v_pk_fma_f32 v[58:59], v[52:53], v[160:161], v[58:59] op_sel_hi:[1,0,0]
	s_nop 2
	v_pk_fma_f32 v[72:73], v[54:55], s[56:57], v[60:61] op_sel_hi:[1,0,1]
	v_pk_fma_f32 v[70:71], v[56:57], s[56:57], v[58:59] op_sel_hi:[1,0,1]
	s_waitcnt lgkmcnt(9)
	v_mfma_f32_16x16x32_bf16 v[56:59], v[120:123], v[46:49], 0
	v_max_f32_e32 v54, v70, v71
	v_max3_f32 v63, v72, v73, v54
	s_or_b64 vcc, s[64:65], s[46:47]
	s_waitcnt lgkmcnt(8)
	v_mfma_f32_16x16x32_bf16 v[54:57], v[124:127], v[42:45], v[56:59]
	s_nop 2
	v_mul_f32_e32 v58, 0x42800000, v160
	v_cndmask_b32_e32 v58, v109, v58, vcc
	v_pk_fma_f32 v[60:61], v[50:51], v[160:161], v[58:59] op_sel_hi:[1,0,0]
	v_pk_fma_f32 v[58:59], v[52:53], v[160:161], v[58:59] op_sel_hi:[1,0,0]
	s_nop 0
	v_pk_fma_f32 v[68:69], v[54:55], s[56:57], v[60:61] op_sel_hi:[1,0,1]
	v_pk_fma_f32 v[66:67], v[56:57], s[56:57], v[58:59] op_sel_hi:[1,0,1]
	s_waitcnt lgkmcnt(7)
	v_mfma_f32_16x16x32_bf16 v[54:57], v[128:131], v[46:49], 0
	v_max_f32_e32 v58, v66, v67
	v_max3_f32 v58, v68, v69, v58
	v_max3_f32 v111, v62, v63, v58
	s_waitcnt lgkmcnt(6)
	v_mfma_f32_16x16x32_bf16 v[54:57], v[132:135], v[42:45], v[54:57]
	v_mul_f32_e32 v58, 0x42400000, v160
	s_or_b64 vcc, s[64:65], s[48:49]
	v_cndmask_b32_e32 v58, v109, v58, vcc
	v_pk_fma_f32 v[60:61], v[50:51], v[160:161], v[58:59] op_sel_hi:[1,0,0]
	v_pk_fma_f32 v[58:59], v[52:53], v[160:161], v[58:59] op_sel_hi:[1,0,0]
	s_nop 2
	v_pk_fma_f32 v[64:65], v[54:55], s[56:57], v[60:61] op_sel_hi:[1,0,1]
	v_pk_fma_f32 v[62:63], v[56:57], s[56:57], v[58:59] op_sel_hi:[1,0,1]
	s_waitcnt lgkmcnt(5)
	v_mfma_f32_16x16x32_bf16 v[56:59], v[136:139], v[46:49], 0
	v_max_f32_e32 v54, v62, v63
	v_max3_f32 v112, v64, v65, v54
	s_or_b64 vcc, s[64:65], s[50:51]
	s_waitcnt lgkmcnt(4)
	v_mfma_f32_16x16x32_bf16 v[54:57], v[140:143], v[42:45], v[56:59]
	s_nop 2
	v_mul_f32_e32 v58, 0x42000000, v160
	v_cndmask_b32_e32 v58, v109, v58, vcc
	v_pk_fma_f32 v[60:61], v[50:51], v[160:161], v[58:59] op_sel_hi:[1,0,0]
	v_pk_fma_f32 v[58:59], v[52:53], v[160:161], v[58:59] op_sel_hi:[1,0,0]
	s_nop 0
	v_pk_fma_f32 v[60:61], v[54:55], s[56:57], v[60:61] op_sel_hi:[1,0,1]
	v_pk_fma_f32 v[58:59], v[56:57], s[56:57], v[58:59] op_sel_hi:[1,0,1]
	s_waitcnt lgkmcnt(3)
	v_mfma_f32_16x16x32_bf16 v[54:57], v[144:147], v[46:49], 0
	v_max_f32_e32 v113, v58, v59
	v_max3_f32 v113, v60, v61, v113
	v_max3_f32 v111, v111, v112, v113
	s_waitcnt lgkmcnt(1)
	v_mfma_f32_16x16x32_bf16 v[46:49], v[152:155], v[46:49], 0
	s_or_b64 vcc, s[64:65], s[52:53]
	v_add_u32_e32 v144, s85, v89
	v_add_u32_e32 v130, v144, v99
	v_mfma_f32_16x16x32_bf16 v[112:115], v[148:151], v[42:45], v[54:57]
	v_add_u32_e32 v140, v144, v100
	v_add_u32_e32 v145, v144, v101
	s_nop 0
	v_mul_f32_e32 v54, 0x41800000, v160
	s_waitcnt lgkmcnt(0)
	v_mfma_f32_16x16x32_bf16 v[42:45], v[156:159], v[42:45], v[46:49]
	s_cmp_eq_u32 s95, 0
	s_cbranch_scc1 .Lcva_skip_l
; #define LAS __attribute__((address_space(3)))
; __device__ __forceinline__ void titem_finish(const TItem& t, int lane, const LAS unsigned char* buf) {
;     const int nblk = t.N / 32, kb = t.item / nblk, nb = t.item % nblk, k0 = 64 * kb, n0 = 32 * nb;
;     const int d0 = t.gmode == 0 ? n0 : ((n0 >> 7) * 256 + (n0 & 127) + (t.gmode == 2 ? 128 : 0));
;     const int c = lane & 7;
;     const LAS float* sb = (const LAS float*)buf;
;     float v[4][8];
;     const float wsc = t.scale;
; #pragma unroll
;     for (int j = 0; j < 4; ++j) { const int n = (lane >> 3) + 8 * j; const LAS float* s = sb + (8 * c) * 32 + 4 * ((n >> 2) ^ c) + (n & 3);
; #pragma unroll
;         for (int q = 0; q < 8; ++q) v[j][q] = s[32 * q] * wsc; }
;     if (t.f8) {
; #pragma unroll
;         for (int j = 0; j < 4; ++j) { const int n = (lane >> 3) + 8 * j;
;             int w0 = __builtin_amdgcn_cvt_pk_fp8_f32(v[j][0], v[j][1], 0, false); w0 = __builtin_amdgcn_cvt_pk_fp8_f32(v[j][2], v[j][3], w0, true);
;             int w1 = __builtin_amdgcn_cvt_pk_fp8_f32(v[j][4], v[j][5], 0, false); w1 = __builtin_amdgcn_cvt_pk_fp8_f32(v[j][6], v[j][7], w1, true);
;             u32x2 o; o.x = (unsigned)w0; o.y = (unsigned)w1;
;             __builtin_nontemporal_store(o, (u32x2*)((unsigned char*)t.WT + (size_t)(d0 + n) * t.K + k0 + 8 * c)); }
	s_waitcnt vmcnt(3)
	v_pk_mul_f32 v[168:169], v[168:169], s[94:95] op_sel_hi:[1,0]
	v_pk_mul_f32 v[170:171], v[170:171], s[94:95] op_sel_hi:[1,0]
	v_pk_mul_f32 v[172:173], v[172:173], s[94:95] op_sel_hi:[1,0]
	v_pk_mul_f32 v[174:175], v[174:175], s[94:95] op_sel_hi:[1,0]
	v_pk_mul_f32 v[176:177], v[176:177], s[94:95] op_sel_hi:[1,0]
	v_pk_mul_f32 v[178:179], v[178:179], s[94:95] op_sel_hi:[1,0]
	v_pk_mul_f32 v[180:181], v[180:181], s[94:95] op_sel_hi:[1,0]
	v_pk_mul_f32 v[182:183], v[182:183], s[94:95] op_sel_hi:[1,0]
	v_pk_mul_f32 v[184:185], v[184:185], s[94:95] op_sel_hi:[1,0]
	v_pk_mul_f32 v[186:187], v[186:187], s[94:95] op_sel_hi:[1,0]
	v_pk_mul_f32 v[188:189], v[188:189], s[94:95] op_sel_hi:[1,0]
	v_pk_mul_f32 v[190:191], v[190:191], s[94:95] op_sel_hi:[1,0]
	v_pk_mul_f32 v[192:193], v[192:193], s[94:95] op_sel_hi:[1,0]
	v_pk_mul_f32 v[194:195], v[194:195], s[94:95] op_sel_hi:[1,0]
	v_pk_mul_f32 v[196:197], v[196:197], s[94:95] op_sel_hi:[1,0]
	v_pk_mul_f32 v[198:199], v[198:199], s[94:95] op_sel_hi:[1,0]
	v_pk_mul_f32 v[200:201], v[200:201], s[94:95] op_sel_hi:[1,0]
	v_pk_mul_f32 v[202:203], v[202:203], s[94:95] op_sel_hi:[1,0]
	v_pk_mul_f32 v[204:205], v[204:205], s[94:95] op_sel_hi:[1,0]
	v_pk_mul_f32 v[206:207], v[206:207], s[94:95] op_sel_hi:[1,0]
	v_pk_mul_f32 v[208:209], v[208:209], s[94:95] op_sel_hi:[1,0]
	v_pk_mul_f32 v[210:211], v[210:211], s[94:95] op_sel_hi:[1,0]
	v_pk_mul_f32 v[212:213], v[212:213], s[94:95] op_sel_hi:[1,0]
	v_pk_mul_f32 v[214:215], v[214:215], s[94:95] op_sel_hi:[1,0]
	v_pk_mul_f32 v[216:217], v[216:217], s[94:95] op_sel_hi:[1,0]
	v_pk_mul_f32 v[218:219], v[218:219], s[94:95] op_sel_hi:[1,0]
	v_pk_mul_f32 v[220:221], v[220:221], s[94:95] op_sel_hi:[1,0]
	v_pk_mul_f32 v[222:223], v[222:223], s[94:95] op_sel_hi:[1,0]
	v_pk_mul_f32 v[224:225], v[224:225], s[94:95] op_sel_hi:[1,0]
	v_pk_mul_f32 v[226:227], v[226:227], s[94:95] op_sel_hi:[1,0]
	v_pk_mul_f32 v[228:229], v[228:229], s[94:95] op_sel_hi:[1,0]
	v_pk_mul_f32 v[230:231], v[230:231], s[94:95] op_sel_hi:[1,0]
	s_lshr_b32 s99, s95, 2
	v_lshlrev_b32_e32 v250, 4, v248
	v_cvt_pk_fp8_f32 v232, v168, v172
	v_cvt_pk_fp8_f32 v233, v184, v188
	v_cvt_pk_fp8_f32 v234, v200, v204
	v_cvt_pk_fp8_f32 v235, v216, v220
	v_cvt_pk_fp8_f32 v236, v169, v173
	v_cvt_pk_fp8_f32 v237, v185, v189
	v_cvt_pk_fp8_f32 v238, v201, v205
	v_cvt_pk_fp8_f32 v239, v217, v221
	v_cvt_pk_fp8_f32 v240, v170, v174
	v_cvt_pk_fp8_f32 v241, v186, v190
	v_cvt_pk_fp8_f32 v242, v202, v206
	v_cvt_pk_fp8_f32 v243, v218, v222
	v_cvt_pk_fp8_f32 v244, v171, v175
	v_cvt_pk_fp8_f32 v245, v187, v191
	v_cvt_pk_fp8_f32 v246, v203, v207
	v_cvt_pk_fp8_f32 v247, v219, v223
	v_mad_u32_u24 v250, v249, s99, v250
	v_add_u32_e32 v251, s95, v250
	v_add_u32_e32 v254, s95, v251
	v_add_u32_e32 v255, s95, v254
	v_cvt_pk_fp8_f32 v232, v176, v180 op_sel:[0,0,1]
	v_cvt_pk_fp8_f32 v233, v192, v196 op_sel:[0,0,1]
	v_cvt_pk_fp8_f32 v234, v208, v212 op_sel:[0,0,1]
	v_cvt_pk_fp8_f32 v235, v224, v228 op_sel:[0,0,1]
	v_cvt_pk_fp8_f32 v236, v177, v181 op_sel:[0,0,1]
	v_cvt_pk_fp8_f32 v237, v193, v197 op_sel:[0,0,1]
	v_cvt_pk_fp8_f32 v238, v209, v213 op_sel:[0,0,1]
	v_cvt_pk_fp8_f32 v239, v225, v229 op_sel:[0,0,1]
	v_cvt_pk_fp8_f32 v240, v178, v182 op_sel:[0,0,1]
	v_cvt_pk_fp8_f32 v241, v194, v198 op_sel:[0,0,1]
	v_cvt_pk_fp8_f32 v242, v210, v214 op_sel:[0,0,1]
	v_cvt_pk_fp8_f32 v243, v226, v230 op_sel:[0,0,1]
	v_cvt_pk_fp8_f32 v244, v179, v183 op_sel:[0,0,1]
	v_cvt_pk_fp8_f32 v245, v195, v199 op_sel:[0,0,1]
	v_cvt_pk_fp8_f32 v246, v211, v215 op_sel:[0,0,1]
	v_cvt_pk_fp8_f32 v247, v227, v231 op_sel:[0,0,1]
	global_store_dwordx4 v250, v[232:235], s[92:93] nt
	global_store_dwordx4 v251, v[236:239], s[92:93] nt
	global_store_dwordx4 v254, v[240:243], s[92:93] nt
	global_store_dwordx4 v255, v[244:247], s[92:93] nt
; #define LAS __attribute__((address_space(3)))
; __device__ __forceinline__ void convert_experts(Frame& F, int lo, int hi) {
;     ...
;     constexpr int NPAIRS = CONV_ITEMS / 2;
;     (void)lo; (void)hi;
; __device__ __forceinline__ void phase_attn(Frame& F) {
;     ...
;             LAS unsigned char* ob = F.lds + (buf ^ 1) * ABUF;
; #pragma unroll
;             for (int jj = 0; jj < 4; ++jj) { const int ch = tid + 512 * jj, row = ch >> 3, c16 = ch & 7;
;                 *(LAS u32x4*)(ob + row * ATT_ROWB + c16 * 16) = kr[jj]; *(LAS u32x4*)(ob + ATT_VOFF + row * ATT_ROWB + c16 * 16) = vr[jj]; }
;         }
;         const AttnUnit nu = un;
;         un = attn_decode(x8 * PER_X + (jl + 2 * G8 < jlast ? jl + 2 * G8 : jlast)); attn_issue(qkv, un, tid, kr, vr);
;         { const char* qb = (const char*)qkv + (((size_t)nu.b * SEQ + nu.r) * NPROJ + nu.h * 64) * 2; const unsigned qo = __umul24((unsigned)(128 * nu.n + ql), (unsigned)nu.d * (NPROJ * 2)) + 16u * fq;
;           qn0 = *(const bf16x8*)(qb + qo); qn1 = *(const bf16x8*)(qb + qo + 64); }
.Lcva_skip_l:
	s_add_i32 s37, s77, s70
	s_xor_b32 s79, s79, 1
	s_min_i32 s37, s37, s71
	s_mul_i32 s58, s79, 0x12000
	s_add_i32 s37, s37, s3
	v_add_u32_e32 v2, s58, v84
	s_mul_hi_i32 s58, s37, 0x2aaaaaab
	s_lshr_b32 s59, s58, 31
	s_ashr_i32 s58, s58, 4
	s_add_i32 s59, s58, s59
	s_mul_i32 s58, s59, 0x60
	s_sub_i32 s37, s37, s58
	s_ashr_i32 s58, s59, 3
	s_and_b32 s80, s59, 7
	v_add_u32_e32 v3, v2, v83
	s_cmp_gt_i32 s37, 31
	ds_write_b128 v3, v[38:41]
	ds_write_b128 v3, v[34:37] offset:36864
	v_add_u32_e32 v3, v2, v85
	s_cselect_b64 s[82:83], -1, 0
	s_cmp_gt_i32 s37, 63
	ds_write_b128 v3, v[30:33]
	ds_write_b128 v3, v[26:29] offset:36864
	v_add_u32_e32 v3, v2, v87
	v_add_u32_e32 v2, v2, v88
	s_cselect_b64 s[86:87], -1, 0
	ds_write_b128 v3, v[22:25]
	ds_write_b128 v3, v[18:21] offset:36864
	ds_write_b128 v2, v[14:17]
	ds_write_b128 v2, v[10:13] offset:36864
	v_cndmask_b32_e64 v2, 0, 1, s[86:87]
	s_cmp_lg_u64 s[82:83], 0
	v_readfirstlane_b32 s59, v2
	s_addc_u32 s81, s59, 0
	s_lshl_b32 s59, s81, 5
	s_lshl_b32 s82, s81, 1
	s_sub_i32 s37, s37, s59
	s_sub_i32 s59, 5, s82
	s_ashr_i32 s83, s37, s59
	s_lshl_b32 s59, -1, s59
	s_andn2_b32 s84, s37, s59
	s_ashr_i32 s59, s58, 31
	s_lshl_b64 s[86:87], s[58:59], 12
	s_ashr_i32 s37, s83, 31
	s_add_u32 s59, s86, s83
	s_addc_u32 s37, s87, s37
	s_mulk_i32 s37, 0xa00
	s_mul_hi_u32 s86, s59, 0xa00
	s_add_i32 s87, s86, s37
	s_mulk_i32 s59, 0xa00
	s_lshl_b32 s37, s80, 6
	s_or_b32 s86, s59, s37
	s_lshl_b64 s[86:87], s[86:87], 1
	s_add_u32 s37, s33, s86
	s_addc_u32 s59, s66, s87
	s_add_u32 s86, s37, 0x400
	s_addc_u32 s87, s59, 0
	s_lshl_b32 s59, s84, 7
	v_add_u32_e32 v2, s59, v81
	s_lshl_b32 s37, 0x1400, s82
	v_max_i32_e32 v3, 0, v2
	v_mul_u32_u24_e32 v3, s37, v3
	v_or_b32_e32 v3, v3, v80
	global_load_dwordx4 v[38:41], v3, s[86:87]
	global_load_dwordx4 v[34:37], v3, s[86:87] offset:1024
	v_max_i32_e32 v3, 0xffffffc0, v2
	v_add_u32_e32 v3, 64, v3
	v_mul_u32_u24_e32 v3, s37, v3
	v_or_b32_e32 v3, v3, v80
	global_load_dwordx4 v[30:33], v3, s[86:87]
	global_load_dwordx4 v[26:29], v3, s[86:87] offset:1024
	v_add_u32_e32 v3, s59, v1
	v_max_i32_e32 v2, 0xffffff40, v2
	v_max_i32_e32 v3, 0, v3
	v_add_u32_e32 v2, 0xc0, v2
	v_mul_u32_u24_e32 v3, s37, v3
	v_mul_u32_u24_e32 v2, s37, v2
	v_or_b32_e32 v3, v3, v80
	v_or_b32_e32 v2, v2, v80
	s_ashr_i32 s37, s36, 31
	global_load_dwordx4 v[22:25], v3, s[86:87]
	global_load_dwordx4 v[18:21], v3, s[86:87] offset:1024
	global_load_dwordx4 v[14:17], v2, s[86:87]
	global_load_dwordx4 v[10:13], v2, s[86:87] offset:1024
	s_lshl_b64 s[86:87], s[36:37], 12
	s_ashr_i32 s37, s73, 31
	s_add_u32 s59, s86, s73
	s_addc_u32 s37, s87, s37
	s_mulk_i32 s37, 0xa00
	s_mul_hi_u32 s86, s59, 0xa00
	s_add_i32 s87, s86, s37
	s_mulk_i32 s59, 0xa00
	s_lshl_b32 s37, s75, 6
	s_or_b32 s86, s59, s37
	s_lshl_b64 s[86:87], s[86:87], 1
	s_add_u32 s86, s33, s86
	s_addc_u32 s87, s66, s87
	s_lshl_b32 s37, 0x1400, s74
	v_lshl_add_u32 v2, s76, 7, v86
	s_and_b32 s37, s37, 0x555400
	v_mul_u32_u24_e32 v2, s37, v2
	v_or_b32_e32 v6, v2, v82
	global_load_dwordx4 v[2:5], v6, s[86:87]
	s_nop 0
	global_load_dwordx4 v[6:9], v6, s[86:87] offset:64
	s_and_b32 s98, s32, 3
	s_add_u32 s32, s32, 1
	s_cmp_eq_u32 s98, 0
	s_cbranch_scc0 .Lcva_dummy_l
	s_cmp_eq_u32 s90, 0
	s_cbranch_scc1 .Lcva_dummy_l
	s_sub_u32 s90, s90, 1
	s_lshr_b32 s98, s89, 6
	s_and_b32 s99, s89, 63
	s_mul_hi_u32 s100, s98, 0xaaaaaaab
	s_lshr_b32 s100, s100, 1
	s_mul_i32 s101, s100, 3
	s_sub_u32 s101, s98, s101
	s_cmp_lt_u32 s100, 256
	s_cselect_b32 s98, 0, 3
	s_cselect_b32 s95, s100, 0
	s_add_u32 s98, s98, s101
	s_lshl_b32 s98, s98, 1
	v_readlane_b32 s96, v253, s98
	s_add_u32 s98, s98, 1
	v_readlane_b32 s97, v253, s98
	s_lshl_b32 s95, s95, 20
	s_nop 3
	s_add_u32 s96, s96, s95
	s_addc_u32 s97, s97, 0
	s_cmp_eq_u32 s101, 2
	s_cbranch_scc1 .Lcva_down_l
	s_lshr_b32 s95, s99, 3
	s_and_b32 s99, s99, 7
	s_lshl_b32 s98, s95, 17
	s_add_u32 s96, s96, s98
	s_addc_u32 s97, s97, 0
	s_lshl_b32 s98, s99, 7
	s_add_u32 s96, s96, s98
	s_addc_u32 s97, s97, 0
	s_lshl_b32 s100, s100, 19
	s_lshr_b32 s98, s99, 2
	s_lshl_b32 s98, s98, 18
	s_add_u32 s100, s100, s98
	s_and_b32 s98, s99, 3
	s_lshl_b32 s98, s98, 15
	s_add_u32 s100, s100, s98
	s_lshl_b32 s98, s101, 17
	s_add_u32 s100, s100, s98
	s_lshl_b32 s98, s95, 7
	s_add_u32 s100, s100, s98
	v_readlane_b32 s92, v253, 12
	v_readlane_b32 s93, v253, 13
	s_mov_b32 s94, 0xc3317218
	s_cmp_eq_u32 s101, 0
	s_cselect_b32 s94, 0xc2b8aa3b, s94
	s_nop 3
	s_add_u32 s92, s92, s100
	s_addc_u32 s93, s93, 0
	s_movk_i32 s95, 0x400
	s_movk_i32 s98, 0x400
	s_branch .Lcva_go_l

; #define LAS __attribute__((address_space(3)))
; __device__ __forceinline__ float fast_exp2(float x) { return __builtin_amdgcn_exp2f(x); }
; __device__ __forceinline__ void titem_issue(const TItem& t, int lane, LAS unsigned char* buf) {
;     const int nblk = t.N / 32, kb = t.item / nblk, nb = t.item % nblk, k0 = 64 * kb, n0 = 32 * nb;
; #pragma unroll
;     for (int j = 0; j < 8; ++j) { const float* g = t.W + (size_t)(k0 + 8 * j + (lane >> 3)) * t.N + n0 + 4 * ((lane & 7) ^ j);
;         __builtin_amdgcn_global_load_lds((const unsigned*)g, (LAS unsigned*)(buf + j * 1024), 16, 0, 2); }
; }
; __device__ __forceinline__ void phase_attn(Frame& F) {
;     ...
;             const float kT = (!first || w + T >= 8) ? nc2 * (float)(128 - 16 * T) : -INFINITY;
;             sa = sa * c1 + (eb + kT);
; #pragma unroll
;             for (int rg = 0; rg < 4; ++rg) {
;                 if (T == 0) sa[rg] = ef[rg] <= 0.f ? sa[rg] : -INFINITY;
;                 if (T == 8) sa[rg] = ef[rg] >= 0.f ? sa[rg] : -INFINITY;
;             }
;             St[T] = sa;
;             mx = fmaxf(mx, fmaxf(fmaxf(sa[0], sa[1]), fmaxf(sa[2], sa[3])));
;         }
;         mx = fmaxf(mx, __shfl_xor(mx, 16)); mx = fmaxf(mx, __shfl_xor(mx, 32));
;         f32x4 lv = (f32x4){0.f, 0.f, 0.f, 0.f};
;         f32x4 nmx = (f32x4){-mx, -mx, -mx, -mx}; asm volatile("" : "+v"(nmx));
; #pragma unroll
;         for (int T = 0; T < 9; ++T) { const f32x4 d = St[T] + nmx; f32x4 pv; pv.x = fast_exp2(d.x); pv.y = fast_exp2(d.y); pv.z = fast_exp2(d.z); pv.w = fast_exp2(d.w); St[T] = pv; lv = lv + pv; }
;         float l = (lv.x + lv.y) + (lv.z + lv.w);
;         l += __shfl_xor(l, 16); l += __shfl_xor(l, 32);
;         f32x4 O[4];
; #pragma unroll
;         for (int dt = 0; dt < 4; ++dt) O[dt] = (f32x4){0.f, 0.f, 0.f, 0.f};
; #pragma unroll
;         for (int T = 0; T < 9; ++T) {
;             u32x2 pw; pw.x = cvt_pk_bf16(St[T][0], St[T][1]); pw.y = cvt_pk_bf16(St[T][2], St[T][3]);
;             const s16x4 pb = __builtin_bit_cast(s16x4, pw);
;             LAS unsigned char* va = kb + ATT_VOFF + (16 * (w + T) + 4 * fq + (fr >> 2)) * ATT_ROWB + (8 * (fr & 3)) * 2;
; #pragma unroll
;             for (int dt = 0; dt < 4; ++dt) O[dt] = __builtin_amdgcn_mfma_f32_16x16x16bf16_1k(tr_read(va + 64 * (dt >> 1) + 8 * (dt & 1)), pb, O[dt], 0, 0, 0);
.Lcva_go_l:
	s_lshl_b32 s99, s98, 4
	v_mad_u32_u24 v250, v248, s99, v249
	global_load_dwordx4 v[168:171], v250, s[96:97] nt
	s_add_u32 s96, s96, s98
	s_addc_u32 s97, s97, 0
	global_load_dwordx4 v[172:175], v250, s[96:97] nt
	s_add_u32 s96, s96, s98
	s_addc_u32 s97, s97, 0
	global_load_dwordx4 v[176:179], v250, s[96:97] nt
	s_add_u32 s96, s96, s98
	s_addc_u32 s97, s97, 0
	global_load_dwordx4 v[180:183], v250, s[96:97] nt
	s_add_u32 s96, s96, s98
	s_addc_u32 s97, s97, 0
	global_load_dwordx4 v[184:187], v250, s[96:97] nt
	s_add_u32 s96, s96, s98
	s_addc_u32 s97, s97, 0
	global_load_dwordx4 v[188:191], v250, s[96:97] nt
	s_add_u32 s96, s96, s98
	s_addc_u32 s97, s97, 0
	global_load_dwordx4 v[192:195], v250, s[96:97] nt
	s_add_u32 s96, s96, s98
	s_addc_u32 s97, s97, 0
	global_load_dwordx4 v[196:199], v250, s[96:97] nt
	s_add_u32 s96, s96, s98
	s_addc_u32 s97, s97, 0
	global_load_dwordx4 v[200:203], v250, s[96:97] nt
	s_add_u32 s96, s96, s98
	s_addc_u32 s97, s97, 0
	global_load_dwordx4 v[204:207], v250, s[96:97] nt
	s_add_u32 s96, s96, s98
	s_addc_u32 s97, s97, 0
	global_load_dwordx4 v[208:211], v250, s[96:97] nt
	s_add_u32 s96, s96, s98
	s_addc_u32 s97, s97, 0
	global_load_dwordx4 v[212:215], v250, s[96:97] nt
	s_add_u32 s96, s96, s98
	s_addc_u32 s97, s97, 0
	global_load_dwordx4 v[216:219], v250, s[96:97] nt
	s_add_u32 s96, s96, s98
	s_addc_u32 s97, s97, 0
	global_load_dwordx4 v[220:223], v250, s[96:97] nt
	s_add_u32 s96, s96, s98
	s_addc_u32 s97, s97, 0
	global_load_dwordx4 v[224:227], v250, s[96:97] nt
	s_add_u32 s96, s96, s98
	s_addc_u32 s97, s97, 0
	global_load_dwordx4 v[228:231], v250, s[96:97] nt
	s_lshl_b32 s99, s69, 6
	s_cmp_eq_u32 s95, 0
	s_cselect_b32 s99, 0, s99
	s_add_u32 s89, s89, s99
	v_cndmask_b32_e32 v54, v109, v54, vcc
	s_or_b64 vcc, s[64:65], s[54:55]
	v_pk_fma_f32 v[56:57], v[50:51], v[160:161], v[54:55] op_sel_hi:[1,0,0]
	v_mul_f32_e32 v46, 0, v160
	v_cndmask_b32_e32 v46, v109, v46, vcc
	v_pk_fma_f32 v[48:49], v[50:51], v[160:161], v[46:47] op_sel_hi:[1,0,0]
	v_pk_fma_f32 v[46:47], v[52:53], v[160:161], v[46:47] op_sel_hi:[1,0,0]
	v_pk_fma_f32 v[54:55], v[52:53], v[160:161], v[54:55] op_sel_hi:[1,0,0]
	v_pk_fma_f32 v[44:45], v[44:45], s[56:57], v[46:47] op_sel_hi:[1,0,1]
	v_pk_fma_f32 v[42:43], v[42:43], s[56:57], v[48:49] op_sel_hi:[1,0,1]
	v_cndmask_b32_e64 v48, v109, v44, s[18:19]
	v_and_b32_e32 v44, 64, v108
	v_pk_fma_f32 v[54:55], v[114:115], s[56:57], v[54:55] op_sel_hi:[1,0,1]
	v_cndmask_b32_e64 v47, v109, v43, s[16:17]
	v_cndmask_b32_e64 v49, v109, v45, s[20:21]
	v_xor_b32_e32 v43, 16, v108
	v_add_u32_e32 v44, 64, v44
	v_pk_fma_f32 v[56:57], v[112:113], s[56:57], v[56:57] op_sel_hi:[1,0,1]
	v_max_f32_e32 v112, v54, v55
	v_cndmask_b32_e64 v46, v109, v42, s[14:15]
	v_max_f32_e32 v42, v48, v49
	v_cmp_lt_i32_e32 vcc, v43, v44
	v_max3_f32 v112, v56, v57, v112
	v_max3_f32 v42, v46, v47, v42
	v_cndmask_b32_e32 v43, v108, v43, vcc
	v_max3_f32 v42, v111, v112, v42
	v_lshlrev_b32_e32 v142, 2, v43
	ds_bpermute_b32 v43, v142, v42
	s_waitcnt lgkmcnt(0)
	v_max_f32_e32 v43, v43, v43
	v_max_f32_e32 v42, v42, v43
	v_xor_b32_e32 v43, 32, v108
	v_cmp_lt_i32_e32 vcc, v43, v44
	s_nop 1
	v_cndmask_b32_e32 v43, v108, v43, vcc
	v_lshlrev_b32_e32 v143, 2, v43
	ds_bpermute_b32 v43, v143, v42
	s_waitcnt lgkmcnt(0)
	v_max_f32_e32 v43, v43, v43
	v_max_f32_e32 v111, v42, v43
	v_xor_b32_e32 v42, 0x80000000, v111
	v_mov_b32_e32 v43, v42
	v_mov_b32_e32 v44, v42
	v_mov_b32_e32 v45, v42
	ds_read_b64_tr_b16 v[120:121], v130 offset:36864
	v_pk_add_f32 v[118:119], v[166:167], v[44:45]
	v_pk_add_f32 v[112:113], v[164:165], v[44:45]
	v_exp_f32_e32 v126, v118
	v_exp_f32_e32 v127, v119
	ds_read_b64_tr_b16 v[118:119], v130 offset:36872
	v_pk_add_f32 v[114:115], v[162:163], v[42:43]
	v_exp_f32_e32 v112, v112
	v_exp_f32_e32 v114, v114
	v_exp_f32_e32 v113, v113
	v_exp_f32_e32 v115, v115
	ds_read_b64_tr_b16 v[128:129], v130 offset:36928
	ds_read_b64_tr_b16 v[130:131], v130 offset:36936
	v_pk_add_f32 v[134:135], v[76:77], v[42:43]
	v_cvt_pk_bf16_f32 v123, v112, v113
	v_cvt_pk_bf16_f32 v122, v114, v115
	v_pk_add_f32 v[116:117], v[112:113], 0 op_sel_hi:[1,0]
	v_pk_add_f32 v[124:125], v[114:115], 0 op_sel_hi:[1,0]
	s_waitcnt lgkmcnt(3)
	v_mfma_f32_16x16x16_bf16 v[112:115], v[120:121], v[122:123], 0
	v_add_f32_e64 v120, v74, v44
	v_add_f32_e64 v121, v75, v45
	v_pk_add_f32 v[132:133], v[126:127], v[116:117]
	v_exp_f32_e32 v136, v120
	s_waitcnt lgkmcnt(2)
	v_mfma_f32_16x16x16_bf16 v[116:119], v[118:119], v[122:123], 0
	v_exp_f32_e32 v137, v121
	v_pk_add_f32 v[78:79], v[78:79], v[42:43]
	v_cvt_pk_bf16_f32 v139, v126, v127
	s_waitcnt lgkmcnt(1)
	v_mfma_f32_16x16x16_bf16 v[74:77], v[128:129], v[122:123], 0
	ds_read_b64_tr_b16 v[128:129], v140 offset:36864
	v_exp_f32_e32 v78, v78
	v_exp_f32_e32 v79, v79
	s_waitcnt lgkmcnt(1)
	v_mfma_f32_16x16x16_bf16 v[120:123], v[130:131], v[122:123], 0
	ds_read_b64_tr_b16 v[130:131], v140 offset:36872
	ds_read_b64_tr_b16 v[126:127], v140 offset:36928
	ds_read_b64_tr_b16 v[140:141], v140 offset:36936
	v_cvt_pk_bf16_f32 v138, v78, v79
	v_exp_f32_e32 v134, v134
	v_exp_f32_e32 v135, v135
	s_waitcnt lgkmcnt(3)
	v_mfma_f32_16x16x16_bf16 v[112:115], v[128:129], v[138:139], v[112:115]
	v_add_f32_e64 v128, v70, v44
	v_add_f32_e64 v129, v71, v45
	v_pk_add_f32 v[78:79], v[78:79], v[124:125]
	v_pk_add_f32 v[124:125], v[136:137], v[132:133]
	s_waitcnt lgkmcnt(2)
	v_mfma_f32_16x16x16_bf16 v[116:119], v[130:131], v[138:139], v[116:119]
	v_add_f32_e64 v130, v72, v42
	v_add_f32_e64 v131, v73, v43
	v_pk_add_f32 v[78:79], v[134:135], v[78:79]
	v_exp_f32_e32 v128, v128
	s_waitcnt lgkmcnt(1)
; #define LAS __attribute__((address_space(3)))
; __device__ __forceinline__ unsigned cvt_pk_bf16(float lo, float hi) { const f32x2_t v = {lo, hi}; return __builtin_bit_cast(unsigned, __builtin_convertvector(v, bf16x2_t)); }
; __device__ __forceinline__ float fast_exp2(float x) { return __builtin_amdgcn_exp2f(x); }
; __device__ __forceinline__ s16x4 tr_read(LAS unsigned char* p) { return __builtin_bit_cast(s16x4, __builtin_amdgcn_ds_read_tr16_b64_v4i16((LAS s16x4*)p)); }
; __device__ __forceinline__ void phase_attn(Frame& F) {
;     ...
;         for (int T = 0; T < 9; ++T) { const f32x4 d = St[T] + nmx; f32x4 pv; pv.x = fast_exp2(d.x); pv.y = fast_exp2(d.y); pv.z = fast_exp2(d.z); pv.w = fast_exp2(d.w); St[T] = pv; lv = lv + pv; }
;         float l = (lv.x + lv.y) + (lv.z + lv.w);
;         l += __shfl_xor(l, 16); l += __shfl_xor(l, 32);
;         f32x4 O[4];
; #pragma unroll
;         for (int dt = 0; dt < 4; ++dt) O[dt] = (f32x4){0.f, 0.f, 0.f, 0.f};
; #pragma unroll
;         for (int T = 0; T < 9; ++T) {
;             u32x2 pw; pw.x = cvt_pk_bf16(St[T][0], St[T][1]); pw.y = cvt_pk_bf16(St[T][2], St[T][3]);
;             const s16x4 pb = __builtin_bit_cast(s16x4, pw);
;             LAS unsigned char* va = kb + ATT_VOFF + (16 * (w + T) + 4 * fq + (fr >> 2)) * ATT_ROWB + (8 * (fr & 3)) * 2;
; #pragma unroll
;             for (int dt = 0; dt < 4; ++dt) O[dt] = __builtin_amdgcn_mfma_f32_16x16x16bf16_1k(tr_read(va + 64 * (dt >> 1) + 8 * (dt & 1)), pb, O[dt], 0, 0, 0);
	v_mfma_f32_16x16x16_bf16 v[70:73], v[126:127], v[138:139], v[74:77]
	ds_read_b64_tr_b16 v[126:127], v145 offset:36864
	v_exp_f32_e32 v129, v129
	v_pk_add_f32 v[48:49], v[44:45], v[48:49]
	s_waitcnt lgkmcnt(1)
	v_mfma_f32_16x16x16_bf16 v[74:77], v[140:141], v[138:139], v[120:123]
	v_add_f32_e64 v124, v128, v124
	v_add_f32_e64 v125, v129, v125
	s_nop 0
	ds_read_b64_tr_b16 v[120:121], v145 offset:36872
	v_cvt_pk_bf16_f32 v122, v134, v135
	ds_read_b64_tr_b16 v[132:133], v145 offset:36928
	ds_read_b64_tr_b16 v[134:135], v145 offset:36936
	v_cvt_pk_bf16_f32 v123, v136, v137
	v_add_u32_e32 v136, v144, v102
	s_waitcnt lgkmcnt(3)
	v_mfma_f32_16x16x16_bf16 v[112:115], v[126:127], v[122:123], v[112:115]
	v_exp_f32_e32 v126, v130
	v_exp_f32_e32 v127, v131
	v_pk_add_f32 v[130:131], v[68:69], v[42:43]
	s_waitcnt lgkmcnt(2)
	v_mfma_f32_16x16x16_bf16 v[116:119], v[120:121], v[122:123], v[116:119]
	v_add_f32_e64 v120, v66, v44
	v_add_f32_e64 v121, v67, v45
	v_pk_add_f32 v[78:79], v[126:127], v[78:79]
	v_exp_f32_e32 v130, v130
	s_waitcnt lgkmcnt(1)
	v_mfma_f32_16x16x16_bf16 v[66:69], v[132:133], v[122:123], v[70:73]
	ds_read_b64_tr_b16 v[132:133], v136 offset:36864
	v_exp_f32_e32 v120, v120
	v_exp_f32_e32 v121, v121
	s_waitcnt lgkmcnt(1)
	v_mfma_f32_16x16x16_bf16 v[70:73], v[134:135], v[122:123], v[74:77]
	ds_read_b64_tr_b16 v[122:123], v136 offset:36872
	v_cvt_pk_bf16_f32 v134, v126, v127
	v_cvt_pk_bf16_f32 v135, v128, v129
	ds_read_b64_tr_b16 v[128:129], v136 offset:36928
	ds_read_b64_tr_b16 v[136:137], v136 offset:36936
	s_waitcnt lgkmcnt(3)
	v_mfma_f32_16x16x16_bf16 v[74:77], v[132:133], v[134:135], v[112:115]
	v_add_u32_e32 v132, v144, v103
	ds_read_b64_tr_b16 v[126:127], v132 offset:36872
	v_exp_f32_e32 v131, v131
	s_waitcnt lgkmcnt(3)
	v_mfma_f32_16x16x16_bf16 v[112:115], v[122:123], v[134:135], v[116:119]
	ds_read_b64_tr_b16 v[122:123], v132 offset:36864
	v_pk_add_f32 v[124:125], v[120:121], v[124:125]
	v_pk_add_f32 v[78:79], v[130:131], v[78:79]
	v_pk_add_f32 v[116:117], v[62:63], v[44:45]
	v_pk_add_f32 v[118:119], v[64:65], v[42:43]
	s_waitcnt lgkmcnt(3)
	v_mfma_f32_16x16x16_bf16 v[62:65], v[128:129], v[134:135], v[66:69]
	v_exp_f32_e32 v116, v116
	v_exp_f32_e32 v117, v117
	v_cvt_pk_bf16_f32 v128, v130, v131
	v_cvt_pk_bf16_f32 v129, v120, v121
	ds_read_b64_tr_b16 v[120:121], v132 offset:36928
	ds_read_b64_tr_b16 v[130:131], v132 offset:36936
	v_add_u32_e32 v132, v144, v104
	s_waitcnt lgkmcnt(4)
	v_mfma_f32_16x16x16_bf16 v[66:69], v[136:137], v[134:135], v[70:73]
	v_exp_f32_e32 v118, v118
	v_exp_f32_e32 v119, v119
	s_waitcnt lgkmcnt(2)
	v_mfma_f32_16x16x16_bf16 v[70:73], v[122:123], v[128:129], v[74:77]
	v_add_f32_e64 v122, v116, v124
	v_add_f32_e64 v123, v117, v125
	ds_read_b64_tr_b16 v[124:125], v132 offset:36872
	v_pk_add_f32 v[78:79], v[118:119], v[78:79]
	v_mfma_f32_16x16x16_bf16 v[74:77], v[126:127], v[128:129], v[112:115]
	v_cvt_pk_bf16_f32 v127, v116, v117
	v_cvt_pk_bf16_f32 v126, v118, v119
	s_nop 0
	v_pk_add_f32 v[112:113], v[58:59], v[44:45]
	v_pk_add_f32 v[114:115], v[60:61], v[42:43]
	s_waitcnt lgkmcnt(2)
	v_mfma_f32_16x16x16_bf16 v[58:61], v[120:121], v[128:129], v[62:65]
	ds_read_b64_tr_b16 v[120:121], v132 offset:36864
	v_exp_f32_e32 v112, v112
	v_exp_f32_e32 v113, v113
	v_exp_f32_e32 v114, v114
	s_waitcnt lgkmcnt(2)
	v_mfma_f32_16x16x16_bf16 v[62:65], v[130:131], v[128:129], v[66:69]
	ds_read_b64_tr_b16 v[116:117], v132 offset:36928
	ds_read_b64_tr_b16 v[128:129], v132 offset:36936
	v_exp_f32_e32 v115, v115
	v_pk_add_f32 v[118:119], v[112:113], v[122:123]
	v_add_u32_e32 v122, v144, v105
	s_waitcnt lgkmcnt(2)
	v_mfma_f32_16x16x16_bf16 v[66:69], v[120:121], v[126:127], v[70:73]
	ds_read_b64_tr_b16 v[120:121], v122 offset:36872
	v_mfma_f32_16x16x16_bf16 v[70:73], v[124:125], v[126:127], v[74:77]
	s_nop 2
	v_add_f32_e64 v74, v114, v78
	v_add_f32_e64 v75, v115, v79
	v_pk_add_f32 v[76:77], v[54:55], v[44:45]
	v_pk_add_f32 v[78:79], v[56:57], v[42:43]
	s_waitcnt lgkmcnt(2)
	v_mfma_f32_16x16x16_bf16 v[54:57], v[116:117], v[126:127], v[58:61]
	ds_read_b64_tr_b16 v[116:117], v122 offset:36864
	v_cvt_pk_bf16_f32 v114, v114, v115
	v_cvt_pk_bf16_f32 v115, v112, v113
	ds_read_b64_tr_b16 v[112:113], v122 offset:36928
	ds_read_b64_tr_b16 v[122:123], v122 offset:36936
	s_waitcnt lgkmcnt(4)
	v_mfma_f32_16x16x16_bf16 v[58:61], v[128:129], v[126:127], v[62:65]
	v_exp_f32_e32 v76, v76
	v_exp_f32_e32 v77, v77
	v_exp_f32_e32 v78, v78
	s_waitcnt lgkmcnt(2)
	v_mfma_f32_16x16x16_bf16 v[62:65], v[116:117], v[114:115], v[66:69]
	v_exp_f32_e32 v79, v79
	v_pk_add_f32 v[116:117], v[76:77], v[118:119]
	v_mfma_f32_16x16x16_bf16 v[66:69], v[120:121], v[114:115], v[70:73]
	s_nop 2
	v_add_f32_e64 v70, v42, v46
	v_add_f32_e64 v71, v43, v47
	s_waitcnt lgkmcnt(1)
	v_mfma_f32_16x16x16_bf16 v[42:45], v[112:113], v[114:115], v[54:57]
	v_exp_f32_e32 v72, v48
	v_exp_f32_e32 v73, v49
	v_exp_f32_e32 v70, v70
	v_add_u32_e32 v56, v144, v106
	ds_read_b64_tr_b16 v[54:55], v56 offset:36864
	s_waitcnt lgkmcnt(1)
	v_mfma_f32_16x16x16_bf16 v[46:49], v[122:123], v[114:115], v[58:61]
	v_exp_f32_e32 v71, v71
	v_cvt_pk_bf16_f32 v112, v78, v79
	v_cvt_pk_bf16_f32 v113, v76, v77
	ds_read_b64_tr_b16 v[58:59], v56 offset:36872
	ds_read_b64_tr_b16 v[76:77], v56 offset:36928
	ds_read_b64_tr_b16 v[114:115], v56 offset:36936
	s_waitcnt lgkmcnt(3)
	v_mfma_f32_16x16x16_bf16 v[54:57], v[54:55], v[112:113], v[62:65]
	s_nop 2
	v_add_f32_e64 v62, v78, v74
	v_add_f32_e64 v63, v79, v75
	v_pk_add_f32 v[64:65], v[72:73], v[116:117]
	v_pk_add_f32 v[62:63], v[70:71], v[62:63]
	v_add_u32_e32 v74, v144, v107
	s_waitcnt lgkmcnt(2)
; #define LAS __attribute__((address_space(3)))
; __device__ __forceinline__ void lds_barrier() { asm volatile("s_waitcnt lgkmcnt(0)\n\ts_barrier" ::: "memory"); }
; __device__ __forceinline__ void phase_attn(Frame& F) {
;     ...
;         l += __shfl_xor(l, 16); l += __shfl_xor(l, 32);
;         f32x4 O[4];
; #pragma unroll
;         for (int dt = 0; dt < 4; ++dt) O[dt] = (f32x4){0.f, 0.f, 0.f, 0.f};
; #pragma unroll
;         for (int T = 0; T < 9; ++T) {
;             u32x2 pw; pw.x = cvt_pk_bf16(St[T][0], St[T][1]); pw.y = cvt_pk_bf16(St[T][2], St[T][3]);
;             const s16x4 pb = __builtin_bit_cast(s16x4, pw);
;             LAS unsigned char* va = kb + ATT_VOFF + (16 * (w + T) + 4 * fq + (fr >> 2)) * ATT_ROWB + (8 * (fr & 3)) * 2;
; #pragma unroll
;             for (int dt = 0; dt < 4; ++dt) O[dt] = __builtin_amdgcn_mfma_f32_16x16x16bf16_1k(tr_read(va + 64 * (dt >> 1) + 8 * (dt & 1)), pb, O[dt], 0, 0, 0);
;         }
;         const float inv = 1.f / l;
;         bf16_t* op = (bf16_t*)((char*)part + (((size_t)cu.dsel * NTOK + (size_t)cu.b * SEQ + cu.r) * 512 + cu.h * 64) * 2 + (qrow * 1024u + 16u * fq));
; #pragma unroll
;         for (int u2 = 0; u2 < 2; ++u2) { u32x4 o4; o4.x = cvt_pk_bf16(O[2 * u2][0] * inv, O[2 * u2][1] * inv); o4.y = cvt_pk_bf16(O[2 * u2][2] * inv, O[2 * u2][3] * inv);
;             o4.z = cvt_pk_bf16(O[2 * u2 + 1][0] * inv, O[2 * u2 + 1][1] * inv); o4.w = cvt_pk_bf16(O[2 * u2 + 1][2] * inv, O[2 * u2 + 1][3] * inv); *(u32x4*)(op + 32 * u2) = o4; }
;         if (fq == 0) *(float*)((char*)lse + (((size_t)cu.dsel * NTOK + (size_t)cu.b * SEQ + cu.r) * 8 + cu.h) * 4 + qrow * 32u) = mx + __builtin_amdgcn_logf(l);
;         cu = nu; buf ^= 1;
;     }
;     __syncthreads();
; __device__ __forceinline__ void phase_sgu(Frame& F) {
;     const bf16_t* qkv = WSP(F, WS_B, bf16_t);
;     bf16_t* sgu = (bf16_t*)F.a->out + (size_t)3 * NTOK * 512;
;     const bf16_t* Wsp = WSP(F, WS_WSP, bf16_t);
;     const float* lng = F.a->in[I_LNG]; const float* lnb = F.a->in[I_LNB]; const float* bsp = F.a->in[I_BSP];
;     const int w = F.wave, lane = F.lane, fr = lane & 15, fq = lane >> 4;
;     for (int un = blockIdx.x; un < NTOK / 128; un += F.G) {
;         const size_t tok0 = (size_t)un * 128;
;         lds_barrier();
;         float g8[8], b8[8];
; #pragma unroll
;         for (int j = 0; j < 8; ++j) { g8[j] = lng[8 * lane + j]; b8[j] = lnb[8 * lane + j]; }
	v_mfma_f32_16x16x16_bf16 v[58:61], v[58:59], v[112:113], v[66:69]
	s_nop 2
	v_pk_mov_b32 v[66:67], v[62:63], v[64:65] op_sel:[1,0]
	v_mov_b32_e32 v63, v65
	ds_read_b64_tr_b16 v[64:65], v74 offset:36864
	v_pk_add_f32 v[62:63], v[66:67], v[62:63]
	v_cvt_pk_bf16_f32 v66, v70, v71
	v_add_f32_e32 v75, v62, v63
	v_cvt_pk_bf16_f32 v67, v72, v73
	s_waitcnt lgkmcnt(2)
	v_mfma_f32_16x16x16_bf16 v[42:45], v[76:77], v[112:113], v[42:45]
	ds_read_b64_tr_b16 v[62:63], v74 offset:36872
	ds_read_b64_tr_b16 v[68:69], v74 offset:36928
	ds_read_b64_tr_b16 v[70:71], v74 offset:36936
	s_waitcnt lgkmcnt(3)
	v_mfma_f32_16x16x16_bf16 v[54:57], v[64:65], v[66:67], v[54:57]
	ds_bpermute_b32 v64, v142, v75
	s_waitcnt lgkmcnt(0)
	v_add_f32_e32 v72, v75, v64
	ds_bpermute_b32 v73, v143, v72
	v_mfma_f32_16x16x16_bf16 v[58:61], v[62:63], v[66:67], v[58:61]
	v_mfma_f32_16x16x16_bf16 v[62:65], v[68:69], v[66:67], v[42:45]
	s_waitcnt lgkmcnt(0)
	s_nop 1
	v_add_f32_e32 v43, v72, v73
	v_div_scale_f32 v68, s[64:65], v43, v43, 1.0
	v_mfma_f32_16x16x16_bf16 v[46:49], v[114:115], v[112:113], v[46:49]
	v_rcp_f32_e32 v69, v68
	v_lshlrev_b32_e32 v42, s35, v110
	s_ashr_i32 s35, s34, 31
	v_mfma_f32_16x16x16_bf16 v[44:47], v[70:71], v[66:67], v[46:49]
	s_lshl_b64 s[64:65], s[26:27], 16
	s_lshl_b64 s[34:35], s[34:35], 12
	s_ashr_i32 s26, s31, 31
	s_nop 0
	v_fma_f32 v48, -v68, v69, 1.0
	v_fmac_f32_e32 v69, v48, v69
	v_div_scale_f32 v48, vcc, 1.0, v43, 1.0
	v_mul_f32_e32 v49, v48, v69
	s_add_u32 s31, s34, s31
	v_fma_f32 v66, -v68, v49, v48
	s_addc_u32 s26, s35, s26
	v_fmac_f32_e32 v49, v66, v69
	s_add_u32 s34, s31, s64
	v_fma_f32 v48, -v68, v49, v48
	s_addc_u32 s35, s26, s65
	v_div_fmas_f32 v48, v48, v69, v49
	s_lshl_b32 s26, s30, 7
	s_lshl_b64 s[64:65], s[34:35], 10
	v_div_fixup_f32 v48, v48, v43, 1.0
	s_add_u32 s31, s24, s64
	v_lshl_or_b32 v49, v42, 10, v82
	s_addc_u32 s37, s25, s65
	v_pk_mul_f32 v[54:55], v[48:49], v[54:55] op_sel_hi:[0,1]
	v_pk_mul_f32 v[56:57], v[48:49], v[56:57] op_sel_hi:[0,1]
	s_add_u32 s64, s31, s26
	v_cvt_pk_bf16_f32 v54, v54, v55
	v_cvt_pk_bf16_f32 v55, v56, v57
	v_pk_mul_f32 v[56:57], v[48:49], v[58:59] op_sel_hi:[0,1]
	v_pk_mul_f32 v[58:59], v[48:49], v[60:61] op_sel_hi:[0,1]
	s_addc_u32 s65, s37, 0
	v_cvt_pk_bf16_f32 v56, v56, v57
	v_cvt_pk_bf16_f32 v57, v58, v59
	global_store_dwordx4 v49, v[54:57], s[64:65]
	v_pk_mul_f32 v[44:45], v[48:49], v[44:45] op_sel_hi:[0,1]
	s_nop 0
	v_pk_mul_f32 v[54:55], v[48:49], v[62:63] op_sel_hi:[0,1]
	v_pk_mul_f32 v[56:57], v[48:49], v[64:65] op_sel_hi:[0,1]
	v_cvt_pk_bf16_f32 v54, v54, v55
	v_cvt_pk_bf16_f32 v55, v56, v57
	v_cvt_pk_bf16_f32 v56, v44, v45
	v_pk_mul_f32 v[44:45], v[48:49], v[46:47] op_sel_hi:[0,1]
	v_cvt_pk_bf16_f32 v57, v44, v45
	global_store_dwordx4 v49, v[54:57], s[64:65] offset:64
	s_and_saveexec_b64 s[64:65], s[4:5]
	s_cbranch_execz .LBB0_303
	s_mov_b32 s31, s27
	v_log_f32_e32 v43, v43
	s_lshl_b64 s[34:35], s[34:35], 5
	s_lshl_b64 s[30:31], s[30:31], 2
	s_add_u32 s26, s67, s34
	s_addc_u32 s34, s68, s35
	s_add_u32 s30, s26, s30
	v_add_f32_e32 v43, v111, v43
	s_addc_u32 s31, s34, s31
	v_lshlrev_b32_e32 v42, 5, v42
	global_store_dword v42, v43, s[30:31]
	s_branch .LBB0_303
.LBB0_306:
	s_waitcnt vmcnt(0)
	s_barrier
.LBB0_307:
	v_mov_b32_e32 v1, v0
	s_cmpk_gt_i32 s2, 0x1ff
	s_mov_b64 s[4:5], s[0:1]
	v_readfirstlane_b32 s6, v1
	s_cbranch_scc1 .LBB0_312
	s_load_dwordx4 s[8:11], s[4:5], 0xb8
	s_load_dword s3, s[28:29], 0x0
	s_waitcnt vmcnt(0)
	v_lshrrev_b32_e32 v6, 1, v1
	v_and_b32_e32 v166, 15, v1
	v_and_b32_e32 v7, 24, v6
	s_waitcnt lgkmcnt(0)
	v_mov_b32_e32 v2, s8
	v_mov_b32_e32 v3, s9
	s_add_u32 s30, s10, 0x151c0000
	s_load_dwordx4 s[12:15], s[4:5], 0x30
	s_load_dwordx2 s[8:9], s[4:5], 0x48
	s_addc_u32 s31, s11, 0
	s_ashr_i32 s4, s6, 2
	s_and_b32 s5, s6, 0xffffff80
	v_and_b32_e32 v5, 63, v1
	s_and_b32 s33, s4, -16
	v_mov_b32_e32 v169, 0
	s_and_b32 s4, s6, 0xffffffc0
	v_bfe_u32 v1, v1, 2, 2
	v_or_b32_e32 v6, s5, v166
	v_lshlrev_b32_e32 v168, 1, v7
	v_or_b32_e32 v14, v7, v1
	v_lshl_add_u64 v[8:9], s[10:11], 0, v[168:169]
	s_mov_b64 s[6:7], 0x70000
	v_or_b32_e32 v10, s4, v7
	v_lshlrev_b32_e32 v12, 5, v5
	v_mov_b32_e32 v13, v169
	v_ashrrev_i32_e32 v7, 31, v6
	v_lshl_add_u64 v[8:9], v[8:9], 0, s[6:7]
	s_waitcnt lgkmcnt(0)
	v_lshl_add_u64 v[170:171], s[12:13], 0, v[12:13]
	v_lshl_add_u64 v[172:173], s[14:15], 0, v[12:13]
	v_lshlrev_b64 v[12:13], 8, v[6:7]
	v_lshl_add_u64 v[174:175], v[8:9], 0, v[12:13]
	v_or_b32_e32 v12, 16, v6
	v_ashrrev_i32_e32 v13, 31, v12
	v_lshlrev_b64 v[12:13], 8, v[12:13]
	v_lshl_add_u64 v[176:177], v[8:9], 0, v[12:13]
	v_or_b32_e32 v12, 32, v6
	v_ashrrev_i32_e32 v13, 31, v12
	v_lshlrev_b64 v[12:13], 8, v[12:13]
	v_lshl_add_u64 v[178:179], v[8:9], 0, v[12:13]
	v_or_b32_e32 v12, 48, v6
	v_ashrrev_i32_e32 v13, 31, v12
	v_lshlrev_b64 v[12:13], 8, v[12:13]
	v_lshl_add_u64 v[180:181], v[8:9], 0, v[12:13]
	v_or_b32_e32 v12, 64, v6
	v_ashrrev_i32_e32 v13, 31, v12
	v_lshlrev_b64 v[12:13], 8, v[12:13]
	v_lshl_add_u64 v[182:183], v[8:9], 0, v[12:13]
	v_or_b32_e32 v12, 0x50, v6
	v_ashrrev_i32_e32 v13, 31, v12
	v_lshlrev_b64 v[12:13], 8, v[12:13]
	v_lshl_add_u64 v[184:185], v[8:9], 0, v[12:13]
	v_or_b32_e32 v12, 0x60, v6
	v_lshlrev_b32_e32 v4, 3, v5
	s_ashr_i32 s5, s4, 31
	v_ashrrev_i32_e32 v13, 31, v12
	s_ashr_i32 s34, s33, 31
	v_and_or_b32 v1, v4, 24, s4
	v_lshlrev_b64 v[12:13], 8, v[12:13]
	s_lshl_b64 s[4:5], s[4:5], 1
	v_lshl_add_u64 v[186:187], v[8:9], 0, v[12:13]
	v_or_b32_e32 v12, 0x70, v6
	s_add_u32 s4, s30, s4
	v_ashrrev_i32_e32 v13, 31, v12
	v_ashrrev_i32_e32 v11, 31, v10
	s_movk_i32 s6, 0x410
	s_addc_u32 s5, s31, s5
	v_lshlrev_b32_e32 v1, 1, v1
	v_lshlrev_b64 v[12:13], 8, v[12:13]
	v_mad_u32_u24 v197, v14, s6, 0
	v_lshl_add_u64 v[206:207], s[4:5], 0, v[168:169]
	v_lshl_add_u64 v[2:3], v[10:11], 1, v[2:3]
	s_mov_b64 s[4:5], 0xc000000
	v_or_b32_e32 v167, 8, v1
	v_or_b32_e32 v193, 64, v1
	v_or_b32_e32 v195, 0x48, v1
	v_lshl_add_u64 v[188:189], v[8:9], 0, v[12:13]
	v_lshl_add_u64 v[190:191], v[6:7], 2, s[8:9]
	v_or_b32_e32 v192, 16, v166
	v_or_b32_e32 v194, 32, v166
	v_or_b32_e32 v196, 48, v166
	v_or_b32_e32 v198, 64, v166
	v_or_b32_e32 v200, 0x50, v166
	v_or_b32_e32 v202, 0x60, v166
	v_or_b32_e32 v204, 0x70, v166
	v_add_u32_e32 v199, 0x10400, v197
	v_add_u32_e32 v201, 0x18600, v197
	v_lshl_add_u32 v203, v5, 4, 0
	v_lshl_add_u64 v[208:209], v[2:3], 0, s[4:5]
	s_movk_i32 s35, 0x1400
	v_lshlrev_b32_e32 v168, 1, v4
	v_mov_b32_e32 v205, 0x358637bd
	s_mov_b32 s36, 0xf800000
	v_mov_b32_e32 v214, 0x260
	v_mov_b32_e32 v215, 0x3b000000
	v_mov_b32_e32 v216, 0x1400
	s_mov_b32 s24, s2

; #define LAS __attribute__((address_space(3)))
; __global__ void __launch_bounds__(NTHR, 2) hybrid_fwd(Args args) {
;     extern __shared__ __attribute__((aligned(16))) unsigned char lds_raw[];
;     LAS unsigned char* const lds = (LAS unsigned char*)lds_raw;
	.amdhsa_kernel _Z10hybrid_fwd4Args
		.amdhsa_group_segment_fixed_size 0
		.amdhsa_private_segment_fixed_size 0
		.amdhsa_kernarg_size 464
		.amdhsa_user_sgpr_count 2
		.amdhsa_user_sgpr_dispatch_ptr 0
		.amdhsa_user_sgpr_queue_ptr 0
		.amdhsa_user_sgpr_kernarg_segment_ptr 1
		.amdhsa_user_sgpr_dispatch_id 0
		.amdhsa_user_sgpr_kernarg_preload_length 0
		.amdhsa_user_sgpr_kernarg_preload_offset 0
		.amdhsa_user_sgpr_private_segment_size 0
		.amdhsa_uses_dynamic_stack 0
		.amdhsa_enable_private_segment 0
		.amdhsa_system_sgpr_workgroup_id_x 1
		.amdhsa_system_sgpr_workgroup_id_y 0
		.amdhsa_system_sgpr_workgroup_id_z 0
		.amdhsa_system_sgpr_workgroup_info 0
		.amdhsa_system_vgpr_workitem_id 0
		.amdhsa_next_free_vgpr 256
		.amdhsa_next_free_sgpr 102
		.amdhsa_accum_offset 256
		.amdhsa_reserve_vcc 1
		.amdhsa_float_round_mode_32 0
		.amdhsa_float_round_mode_16_64 0
		.amdhsa_float_denorm_mode_32 3
		.amdhsa_float_denorm_mode_16_64 3
		.amdhsa_dx10_clamp 1
		.amdhsa_ieee_mode 1
		.amdhsa_fp16_overflow 0
		.amdhsa_tg_split 0
		.amdhsa_exception_fp_ieee_invalid_op 0
		.amdhsa_exception_fp_denorm_src 0
		.amdhsa_exception_fp_ieee_div_zero 0
		.amdhsa_exception_fp_ieee_overflow 0
		.amdhsa_exception_fp_ieee_underflow 0
		.amdhsa_exception_fp_ieee_inexact 0
		.amdhsa_exception_int_div_zero 0
	.end_amdhsa_kernel

; #define LAS __attribute__((address_space(3)))
; __global__ void __launch_bounds__(NTHR, 2) hybrid_fwd(Args args) {
;     extern __shared__ __attribute__((aligned(16))) unsigned char lds_raw[];
;     LAS unsigned char* const lds = (LAS unsigned char*)lds_raw;
amdhsa.kernels:
  - .agpr_count:     0
    .args:
      - .offset:         0
        .size:           208
        .value_kind:     by_value
      - .offset:         208
        .size:           4
        .value_kind:     hidden_block_count_x
      - .offset:         212
        .size:           4
        .value_kind:     hidden_block_count_y
      - .offset:         216
        .size:           4
        .value_kind:     hidden_block_count_z
      - .offset:         220
        .size:           2
        .value_kind:     hidden_group_size_x
      - .offset:         222
        .size:           2
        .value_kind:     hidden_group_size_y
      - .offset:         224
        .size:           2
        .value_kind:     hidden_group_size_z
      - .offset:         226
        .size:           2
        .value_kind:     hidden_remainder_x
      - .offset:         228
        .size:           2
        .value_kind:     hidden_remainder_y
      - .offset:         230
        .size:           2
        .value_kind:     hidden_remainder_z
      - .offset:         248
        .size:           8
        .value_kind:     hidden_global_offset_x
      - .offset:         256
        .size:           8
        .value_kind:     hidden_global_offset_y
      - .offset:         264
        .size:           8
        .value_kind:     hidden_global_offset_z
      - .offset:         272
        .size:           2
        .value_kind:     hidden_grid_dims
      - .offset:         328
        .size:           4
        .value_kind:     hidden_dynamic_lds_size
    .group_segment_fixed_size: 0
    .kernarg_segment_align: 8
    .kernarg_segment_size: 464
    .language:       OpenCL C
    .language_version:
      - 2
      - 0
    .max_flat_workgroup_size: 512
    .name:           _Z10hybrid_fwd4Args
    .private_segment_fixed_size: 0
    .sgpr_count:     108
    .sgpr_spill_count: 35
    .symbol:         _Z10hybrid_fwd4Args.kd
    .uniform_work_group_size: 1
    .uses_dynamic_stack: false
    .vgpr_count:     256
    .vgpr_spill_count: 0
    .wavefront_size: 64
